# LSTM cell update interleaves all four elements of a tile (longer independent chains between dependent transcendentals)
# baseline (speedup 1.0000x reference)
.Lskipy77:
	s_waitcnt lgkmcnt(1)
	ds_read_b128 v[210:213], v243 offset:32
	v_mfma_f32_16x16x32_f16 v[174:177], v[98:101], v[214:217], v[174:177]
	v_mfma_f32_16x16x32_f16 v[178:181], v[102:105], v[214:217], v[178:181]
	v_mfma_f32_16x16x32_f16 v[182:185], v[106:109], v[214:217], v[182:185]
	v_mfma_f32_16x16x32_f16 v[186:189], v[110:113], v[214:217], v[186:189]
	global_load_dwordx4 v[234:237], v246, s[12:13]
	s_waitcnt lgkmcnt(1)
	ds_read_b128 v[214:217], v243 offset:48
	v_mfma_f32_16x16x32_f16 v[174:177], v[114:117], v[206:209], v[174:177]
	v_mfma_f32_16x16x32_f16 v[178:181], v[118:121], v[206:209], v[178:181]
	v_mfma_f32_16x16x32_f16 v[182:185], v[122:125], v[206:209], v[182:185]
	v_mfma_f32_16x16x32_f16 v[186:189], v[126:129], v[206:209], v[186:189]
	global_load_dwordx4 v[238:241], v247, s[8:9]
	s_waitcnt lgkmcnt(1)
	ds_read_b128 v[206:209], v242 offset:2304
	v_mfma_f32_16x16x32_f16 v[174:177], v[130:133], v[210:213], v[174:177]
	v_mfma_f32_16x16x32_f16 v[178:181], v[134:137], v[210:213], v[178:181]
	v_mfma_f32_16x16x32_f16 v[182:185], v[138:141], v[210:213], v[182:185]
	v_mfma_f32_16x16x32_f16 v[186:189], v[142:145], v[210:213], v[186:189]
	s_add_u32 s12, s12, 0x271000
	s_waitcnt lgkmcnt(1)
	ds_read_b128 v[210:213], v242 offset:2320
	v_mfma_f32_16x16x32_f16 v[174:177], v[146:149], v[214:217], v[174:177]
	v_mfma_f32_16x16x32_f16 v[178:181], v[150:153], v[214:217], v[178:181]
	v_mfma_f32_16x16x32_f16 v[182:185], v[154:157], v[214:217], v[182:185]
	v_mfma_f32_16x16x32_f16 v[186:189], v[158:161], v[214:217], v[186:189]
	s_addc_u32 s13, s13, 0
	s_waitcnt lgkmcnt(1)
	ds_read_b128 v[214:217], v242 offset:2400
	v_mfma_f32_16x16x32_f16 v[190:193], v[2:5], v[206:209], v[190:193]
	v_mfma_f32_16x16x32_f16 v[194:197], v[6:9], v[206:209], v[194:197]
	v_mfma_f32_16x16x32_f16 v[198:201], v[10:13], v[206:209], v[198:201]
	v_mfma_f32_16x16x32_f16 v[202:205], v[14:17], v[206:209], v[202:205]
	s_waitcnt lgkmcnt(1)
	ds_read_b128 v[206:209], v242 offset:2336
	v_mfma_f32_16x16x32_f16 v[190:193], v[18:21], v[210:213], v[190:193]
	v_mfma_f32_16x16x32_f16 v[194:197], v[22:25], v[210:213], v[194:197]
	v_mfma_f32_16x16x32_f16 v[198:201], v[26:29], v[210:213], v[198:201]
	v_mfma_f32_16x16x32_f16 v[202:205], v[30:33], v[210:213], v[202:205]
	s_waitcnt lgkmcnt(1)
	ds_read_b128 v[210:213], v242 offset:2352
	v_mfma_f32_16x16x32_f16 v[190:193], v[218:221], v[214:217], v[190:193]
	ds_read_b128 v[218:221], v255 offset:4096
	v_exp_f32_e32 v174, v174
	v_exp_f32_e32 v175, v175
	v_mfma_f32_16x16x32_f16 v[194:197], v[222:225], v[214:217], v[194:197]
	ds_read_b128 v[222:225], v255 offset:5120
	v_exp_f32_e32 v176, v176
	v_exp_f32_e32 v177, v177
	v_mfma_f32_16x16x32_f16 v[198:201], v[226:229], v[214:217], v[198:201]
	ds_read_b128 v[226:229], v255 offset:6144
	v_exp_f32_e32 v178, v178
	v_exp_f32_e32 v179, v179
	v_mfma_f32_16x16x32_f16 v[202:205], v[230:233], v[214:217], v[202:205]
	ds_read_b128 v[230:233], v255 offset:7168
	v_exp_f32_e32 v180, v180
	v_exp_f32_e32 v181, v181
	s_waitcnt lgkmcnt(5)
	ds_read_b128 v[214:217], v243 offset:1280
	v_mfma_f32_16x16x32_f16 v[190:193], v[34:37], v[206:209], v[190:193]
	v_exp_f32_e32 v182, v182
	v_exp_f32_e32 v183, v183
	v_mfma_f32_16x16x32_f16 v[194:197], v[38:41], v[206:209], v[194:197]
	v_exp_f32_e32 v184, v184
	v_exp_f32_e32 v185, v185
	v_mfma_f32_16x16x32_f16 v[198:201], v[42:45], v[206:209], v[198:201]
	v_exp_f32_e32 v186, v186
	v_exp_f32_e32 v187, v187
	v_mfma_f32_16x16x32_f16 v[202:205], v[46:49], v[206:209], v[202:205]
	v_exp_f32_e32 v188, v188
	v_exp_f32_e32 v189, v189
	v_add_f32_e32 v182, 1.0, v182
	s_waitcnt lgkmcnt(5)
	ds_read_b128 v[206:209], v243 offset:1296
	v_mfma_f32_16x16x32_f16 v[190:193], v[50:53], v[210:213], v[190:193]
	v_add_f32_e32 v183, 1.0, v183
	v_add_f32_e32 v184, 1.0, v184
	v_mfma_f32_16x16x32_f16 v[194:197], v[54:57], v[210:213], v[194:197]
	v_add_f32_e32 v185, 1.0, v185
	v_add_f32_e32 v178, 1.0, v178
	v_mfma_f32_16x16x32_f16 v[198:201], v[58:61], v[210:213], v[198:201]
	v_add_f32_e32 v179, 1.0, v179
	v_add_f32_e32 v180, 1.0, v180
	v_mfma_f32_16x16x32_f16 v[202:205], v[62:65], v[210:213], v[202:205]
	v_add_f32_e32 v181, 1.0, v181
	v_fma_f32 v174, v174, v182, v182
	v_fma_f32 v175, v175, v183, v183
	s_waitcnt lgkmcnt(1)
	ds_read_b128 v[210:213], v242 offset:2416
	v_mfma_f32_16x16x32_f16 v[190:193], v[98:101], v[214:217], v[190:193]
	v_fma_f32 v176, v176, v184, v184
	v_fma_f32 v177, v177, v185, v185
	v_mfma_f32_16x16x32_f16 v[194:197], v[102:105], v[214:217], v[194:197]
	v_rcp_f32_e32 v178, v178
	v_rcp_f32_e32 v179, v179
	v_mfma_f32_16x16x32_f16 v[198:201], v[106:109], v[214:217], v[198:201]
	v_rcp_f32_e32 v180, v180
	v_rcp_f32_e32 v181, v181
	v_mfma_f32_16x16x32_f16 v[202:205], v[110:113], v[214:217], v[202:205]
	v_fma_f32 v182, v182, v252, s16
	v_fma_f32 v183, v183, v252, s16
	v_fma_f32 v184, v184, v252, s16
	s_waitcnt lgkmcnt(1)
	ds_read_b128 v[214:217], v242 offset:2368
	v_mfma_f32_16x16x32_f16 v[190:193], v[114:117], v[206:209], v[190:193]
	v_fma_f32 v185, v185, v252, s16
	v_rcp_f32_e32 v174, v174
	v_mfma_f32_16x16x32_f16 v[194:197], v[118:121], v[206:209], v[194:197]
	v_rcp_f32_e32 v175, v175
	v_rcp_f32_e32 v176, v176
	v_mfma_f32_16x16x32_f16 v[198:201], v[122:125], v[206:209], v[198:201]
	v_rcp_f32_e32 v177, v177
	v_mul_f32_e32 v162, v162, v178
	v_mfma_f32_16x16x32_f16 v[202:205], v[126:129], v[206:209], v[202:205]
	v_mul_f32_e32 v163, v163, v179
	v_mul_f32_e32 v164, v164, v180
	s_waitcnt lgkmcnt(1)
	ds_read_b128 v[206:209], v242 offset:2384
	v_mfma_f32_16x16x32_f16 v[190:193], v[218:221], v[210:213], v[190:193]
	ds_read_b128 v[218:221], v255 offset:0
	v_mul_f32_e32 v165, v165, v181
	v_fma_f32 v162, v182, v174, v162
	v_mfma_f32_16x16x32_f16 v[194:197], v[222:225], v[210:213], v[194:197]
	ds_read_b128 v[222:225], v255 offset:1024
	v_fma_f32 v163, v183, v175, v163
	v_fma_f32 v164, v184, v176, v164
	v_mfma_f32_16x16x32_f16 v[198:201], v[226:229], v[210:213], v[198:201]
	ds_read_b128 v[226:229], v255 offset:2048
	v_fma_f32 v165, v185, v177, v165
	v_exp_f32_e32 v178, v162
	v_mfma_f32_16x16x32_f16 v[202:205], v[230:233], v[210:213], v[202:205]
	ds_read_b128 v[230:233], v255 offset:3072
	v_exp_f32_e32 v179, v163
	v_exp_f32_e32 v180, v164
	v_exp_f32_e32 v181, v165
	s_waitcnt lgkmcnt(5)
	ds_read_b128 v[210:213], v243 offset:1312
	v_mfma_f32_16x16x32_f16 v[190:193], v[66:69], v[214:217], v[190:193]
	v_add_f32_e32 v174, 1.0, v178
	v_add_f32_e32 v175, 1.0, v179
	v_mfma_f32_16x16x32_f16 v[194:197], v[70:73], v[214:217], v[194:197]
	v_add_f32_e32 v176, 1.0, v180
	v_add_f32_e32 v177, 1.0, v181
	v_mfma_f32_16x16x32_f16 v[198:201], v[74:77], v[214:217], v[198:201]
	v_add_f32_e32 v182, -1.0, v178
	v_add_f32_e32 v183, -1.0, v179
	v_mfma_f32_16x16x32_f16 v[202:205], v[78:81], v[214:217], v[202:205]
	v_add_f32_e32 v184, -1.0, v180
	v_add_f32_e32 v185, -1.0, v181
	v_fma_f32 v186, v186, v174, v174
	s_waitcnt lgkmcnt(5)
	ds_read_b128 v[214:217], v243 offset:1328
	v_mfma_f32_16x16x32_f16 v[190:193], v[82:85], v[206:209], v[190:193]
	s_waitcnt vmcnt(0)
	ds_write_b128 v249, v[234:237] offset:0
	ds_write_b128 v249, v[238:241] offset:29952
	global_load_dwordx4 v[234:237], v248, s[8:9]
	s_add_u32 s8, s8, 0x271000
	s_addc_u32 s9, s9, 0
	v_fma_f32 v187, v187, v175, v175
	v_mfma_f32_16x16x32_f16 v[194:197], v[86:89], v[206:209], v[194:197]
	v_fma_f32 v188, v188, v176, v176
	v_fma_f32 v189, v189, v177, v177
	v_rcp_f32_e32 v186, v186
	v_mfma_f32_16x16x32_f16 v[198:201], v[90:93], v[206:209], v[198:201]
	v_rcp_f32_e32 v187, v187
	v_rcp_f32_e32 v188, v188
	v_mfma_f32_16x16x32_f16 v[202:205], v[94:97], v[206:209], v[202:205]
	v_rcp_f32_e32 v189, v189
	v_mul_f32_e32 v186, v182, v186
	v_mul_f32_e32 v187, v183, v187
	s_waitcnt lgkmcnt(3)
	ds_read_b128 v[206:209], v242 offset:4608
	v_mfma_f32_16x16x32_f16 v[190:193], v[130:133], v[210:213], v[190:193]
	v_mul_f32_e32 v188, v184, v188
	v_mul_f32_e32 v189, v185, v189
	v_mfma_f32_16x16x32_f16 v[194:197], v[134:137], v[210:213], v[194:197]
	v_cvt_pk_f16_f32 v186, v186, v187
	v_cvt_pk_f16_f32 v187, v188, v189
	v_mfma_f32_16x16x32_f16 v[198:201], v[138:141], v[210:213], v[198:201]
	ds_write_b64 v244, v[186:187] offset:15360
	ds_read_b128 v[174:177], v245 offset:0
	v_mfma_f32_16x16x32_f16 v[202:205], v[142:145], v[210:213], v[202:205]
	ds_read_b128 v[178:181], v245 offset:512
	ds_read_b128 v[182:185], v245 offset:1024
	ds_read_b128 v[186:189], v245 offset:1536
	s_waitcnt lgkmcnt(8)
	ds_read_b128 v[210:213], v242 offset:4624
	v_mfma_f32_16x16x32_f16 v[190:193], v[146:149], v[214:217], v[190:193]
	v_mfma_f32_16x16x32_f16 v[194:197], v[150:153], v[214:217], v[194:197]
	v_mfma_f32_16x16x32_f16 v[198:201], v[154:157], v[214:217], v[198:201]
	v_mfma_f32_16x16x32_f16 v[202:205], v[158:161], v[214:217], v[202:205]
	s_waitcnt lgkmcnt(6)
	ds_read_b128 v[214:217], v242 offset:4704
	s_waitcnt lgkmcnt(5)
	v_mfma_f32_16x16x32_f16 v[174:177], v[2:5], v[206:209], v[174:177]
	s_waitcnt lgkmcnt(4)
	v_mfma_f32_16x16x32_f16 v[178:181], v[6:9], v[206:209], v[178:181]
	s_waitcnt lgkmcnt(3)
	v_mfma_f32_16x16x32_f16 v[182:185], v[10:13], v[206:209], v[182:185]
	s_waitcnt lgkmcnt(2)
	v_mfma_f32_16x16x32_f16 v[186:189], v[14:17], v[206:209], v[186:189]
	s_waitcnt lgkmcnt(1)
	ds_read_b128 v[206:209], v242 offset:4640
	v_mfma_f32_16x16x32_f16 v[174:177], v[18:21], v[210:213], v[174:177]
	v_mfma_f32_16x16x32_f16 v[178:181], v[22:25], v[210:213], v[178:181]
	v_mfma_f32_16x16x32_f16 v[182:185], v[26:29], v[210:213], v[182:185]
	v_mfma_f32_16x16x32_f16 v[186:189], v[30:33], v[210:213], v[186:189]
	s_waitcnt lgkmcnt(1)
	ds_read_b128 v[210:213], v242 offset:4656
	v_mfma_f32_16x16x32_f16 v[174:177], v[218:221], v[214:217], v[174:177]
	ds_read_b128 v[218:221], v255 offset:4096
	v_exp_f32_e32 v190, v190
	v_exp_f32_e32 v191, v191
	v_mfma_f32_16x16x32_f16 v[178:181], v[222:225], v[214:217], v[178:181]
	ds_read_b128 v[222:225], v255 offset:5120
	v_exp_f32_e32 v192, v192
	v_exp_f32_e32 v193, v193
	v_mfma_f32_16x16x32_f16 v[182:185], v[226:229], v[214:217], v[182:185]
	ds_read_b128 v[226:229], v255 offset:6144
	v_exp_f32_e32 v194, v194
	v_exp_f32_e32 v195, v195
	v_mfma_f32_16x16x32_f16 v[186:189], v[230:233], v[214:217], v[186:189]
	ds_read_b128 v[230:233], v255 offset:7168
	v_exp_f32_e32 v196, v196
	v_exp_f32_e32 v197, v197
	s_waitcnt lgkmcnt(5)
	ds_read_b128 v[214:217], v243 offset:2560
	v_mfma_f32_16x16x32_f16 v[174:177], v[34:37], v[206:209], v[174:177]
	v_exp_f32_e32 v198, v198
	v_exp_f32_e32 v199, v199
	v_mfma_f32_16x16x32_f16 v[178:181], v[38:41], v[206:209], v[178:181]
	v_exp_f32_e32 v200, v200
	v_exp_f32_e32 v201, v201
	v_mfma_f32_16x16x32_f16 v[182:185], v[42:45], v[206:209], v[182:185]
	v_exp_f32_e32 v202, v202
	v_exp_f32_e32 v203, v203
	v_mfma_f32_16x16x32_f16 v[186:189], v[46:49], v[206:209], v[186:189]
	v_exp_f32_e32 v204, v204
	v_exp_f32_e32 v205, v205
	v_add_f32_e32 v198, 1.0, v198
	s_waitcnt lgkmcnt(5)
	ds_read_b128 v[206:209], v243 offset:2576
	v_mfma_f32_16x16x32_f16 v[174:177], v[50:53], v[210:213], v[174:177]
	v_add_f32_e32 v199, 1.0, v199
	v_add_f32_e32 v200, 1.0, v200
	v_mfma_f32_16x16x32_f16 v[178:181], v[54:57], v[210:213], v[178:181]
	v_add_f32_e32 v201, 1.0, v201
	v_add_f32_e32 v194, 1.0, v194
	v_mfma_f32_16x16x32_f16 v[182:185], v[58:61], v[210:213], v[182:185]
	v_add_f32_e32 v195, 1.0, v195
	v_add_f32_e32 v196, 1.0, v196
	v_mfma_f32_16x16x32_f16 v[186:189], v[62:65], v[210:213], v[186:189]
	v_add_f32_e32 v197, 1.0, v197
	v_fma_f32 v190, v190, v198, v198
	v_fma_f32 v191, v191, v199, v199
	s_waitcnt lgkmcnt(1)
	ds_read_b128 v[210:213], v242 offset:4720
	v_mfma_f32_16x16x32_f16 v[174:177], v[98:101], v[214:217], v[174:177]
	v_fma_f32 v192, v192, v200, v200
	v_fma_f32 v193, v193, v201, v201
	v_mfma_f32_16x16x32_f16 v[178:181], v[102:105], v[214:217], v[178:181]
	v_rcp_f32_e32 v194, v194
	v_rcp_f32_e32 v195, v195
	v_mfma_f32_16x16x32_f16 v[182:185], v[106:109], v[214:217], v[182:185]
	v_rcp_f32_e32 v196, v196
	v_rcp_f32_e32 v197, v197
	v_mfma_f32_16x16x32_f16 v[186:189], v[110:113], v[214:217], v[186:189]
	v_fma_f32 v198, v198, v252, s16
	v_fma_f32 v199, v199, v252, s16
	v_fma_f32 v200, v200, v252, s16
	s_waitcnt lgkmcnt(1)
	ds_read_b128 v[214:217], v242 offset:4672
	v_mfma_f32_16x16x32_f16 v[174:177], v[114:117], v[206:209], v[174:177]
	v_fma_f32 v201, v201, v252, s16
	v_rcp_f32_e32 v190, v190
	v_mfma_f32_16x16x32_f16 v[178:181], v[118:121], v[206:209], v[178:181]
	v_rcp_f32_e32 v191, v191
	v_rcp_f32_e32 v192, v192
	v_mfma_f32_16x16x32_f16 v[182:185], v[122:125], v[206:209], v[182:185]
	v_rcp_f32_e32 v193, v193
	v_mul_f32_e32 v166, v166, v194
	v_mfma_f32_16x16x32_f16 v[186:189], v[126:129], v[206:209], v[186:189]
	v_mul_f32_e32 v167, v167, v195
	v_mul_f32_e32 v168, v168, v196
	s_waitcnt lgkmcnt(1)
	ds_read_b128 v[206:209], v242 offset:4688
	v_mfma_f32_16x16x32_f16 v[174:177], v[218:221], v[210:213], v[174:177]
	ds_read_b128 v[218:221], v255 offset:0
	v_mul_f32_e32 v169, v169, v197
	v_fma_f32 v166, v198, v190, v166
	v_mfma_f32_16x16x32_f16 v[178:181], v[222:225], v[210:213], v[178:181]
	ds_read_b128 v[222:225], v255 offset:1024
	v_fma_f32 v167, v199, v191, v167
	v_fma_f32 v168, v200, v192, v168
	v_mfma_f32_16x16x32_f16 v[182:185], v[226:229], v[210:213], v[182:185]
	ds_read_b128 v[226:229], v255 offset:2048
	v_fma_f32 v169, v201, v193, v169
	v_exp_f32_e32 v194, v166
	v_mfma_f32_16x16x32_f16 v[186:189], v[230:233], v[210:213], v[186:189]
	ds_read_b128 v[230:233], v255 offset:3072
	v_exp_f32_e32 v195, v167
	v_exp_f32_e32 v196, v168
	v_exp_f32_e32 v197, v169
	s_waitcnt lgkmcnt(5)
	ds_read_b128 v[210:213], v243 offset:2592
	v_mfma_f32_16x16x32_f16 v[174:177], v[66:69], v[214:217], v[174:177]
	v_add_f32_e32 v190, 1.0, v194
	v_add_f32_e32 v191, 1.0, v195
	v_mfma_f32_16x16x32_f16 v[178:181], v[70:73], v[214:217], v[178:181]
	v_add_f32_e32 v192, 1.0, v196
	v_add_f32_e32 v193, 1.0, v197
	v_mfma_f32_16x16x32_f16 v[182:185], v[74:77], v[214:217], v[182:185]
	v_add_f32_e32 v198, -1.0, v194
	v_add_f32_e32 v199, -1.0, v195
	v_mfma_f32_16x16x32_f16 v[186:189], v[78:81], v[214:217], v[186:189]
	v_add_f32_e32 v200, -1.0, v196
	v_add_f32_e32 v201, -1.0, v197
	v_fma_f32 v202, v202, v190, v190
	s_waitcnt lgkmcnt(5)
	ds_read_b128 v[214:217], v243 offset:2608
	v_mfma_f32_16x16x32_f16 v[174:177], v[82:85], v[206:209], v[174:177]
	v_fma_f32 v203, v203, v191, v191
	v_fma_f32 v204, v204, v192, v192
	v_mfma_f32_16x16x32_f16 v[178:181], v[86:89], v[206:209], v[178:181]
	v_fma_f32 v205, v205, v193, v193
	v_rcp_f32_e32 v202, v202
	v_mfma_f32_16x16x32_f16 v[182:185], v[90:93], v[206:209], v[182:185]
	v_rcp_f32_e32 v203, v203
	v_rcp_f32_e32 v204, v204
	v_mfma_f32_16x16x32_f16 v[186:189], v[94:97], v[206:209], v[186:189]
	v_rcp_f32_e32 v205, v205
	v_mul_f32_e32 v202, v198, v202
	v_mul_f32_e32 v203, v199, v203
	s_waitcnt lgkmcnt(1)
	ds_read_b128 v[206:209], v242 offset:27648
	v_mfma_f32_16x16x32_f16 v[174:177], v[130:133], v[210:213], v[174:177]
	v_mul_f32_e32 v204, v200, v204
	v_mul_f32_e32 v205, v201, v205
	v_mfma_f32_16x16x32_f16 v[178:181], v[134:137], v[210:213], v[178:181]
	v_cvt_pk_f16_f32 v202, v202, v203
	v_cvt_pk_f16_f32 v203, v204, v205
	v_mfma_f32_16x16x32_f16 v[182:185], v[138:141], v[210:213], v[182:185]
	ds_write_b64 v244, v[202:203] offset:16640
	ds_read_b128 v[190:193], v245 offset:0
	v_mfma_f32_16x16x32_f16 v[186:189], v[142:145], v[210:213], v[186:189]
	ds_read_b128 v[194:197], v245 offset:512
	ds_read_b128 v[198:201], v245 offset:1024
	ds_read_b128 v[202:205], v245 offset:1536
	s_waitcnt lgkmcnt(6)
	ds_read_b128 v[210:213], v242 offset:27744
	v_mfma_f32_16x16x32_f16 v[174:177], v[146:149], v[214:217], v[174:177]
	v_mfma_f32_16x16x32_f16 v[178:181], v[150:153], v[214:217], v[178:181]
	v_mfma_f32_16x16x32_f16 v[182:185], v[154:157], v[214:217], v[182:185]
	v_mfma_f32_16x16x32_f16 v[186:189], v[158:161], v[214:217], v[186:189]
	s_waitcnt vmcnt(0)
	ds_write_b128 v249, v[234:237] offset:32256
	s_waitcnt lgkmcnt(7)
	ds_read_b128 v[214:217], v242 offset:27664
	s_waitcnt lgkmcnt(6)
	v_mfma_f32_16x16x32_f16 v[190:193], v[2:5], v[206:209], v[190:193]
	s_waitcnt lgkmcnt(5)
	v_mfma_f32_16x16x32_f16 v[194:197], v[6:9], v[206:209], v[194:197]
	s_waitcnt lgkmcnt(4)
	v_mfma_f32_16x16x32_f16 v[198:201], v[10:13], v[206:209], v[198:201]
	s_waitcnt lgkmcnt(3)
	v_mfma_f32_16x16x32_f16 v[202:205], v[14:17], v[206:209], v[202:205]
	s_waitcnt lgkmcnt(2)
	ds_read_b128 v[206:209], v242 offset:27680
	v_mfma_f32_16x16x32_f16 v[190:193], v[218:221], v[210:213], v[190:193]
	ds_read_b128 v[218:221], v255 offset:4096
	v_exp_f32_e32 v174, v174
	v_exp_f32_e32 v175, v175
	v_exp_f32_e32 v176, v176
	v_mfma_f32_16x16x32_f16 v[194:197], v[222:225], v[210:213], v[194:197]
	ds_read_b128 v[222:225], v255 offset:5120
	v_exp_f32_e32 v177, v177
	v_exp_f32_e32 v178, v178
	v_exp_f32_e32 v179, v179
	v_exp_f32_e32 v180, v180
	v_mfma_f32_16x16x32_f16 v[198:201], v[226:229], v[210:213], v[198:201]
	ds_read_b128 v[226:229], v255 offset:6144
	v_exp_f32_e32 v181, v181
	v_exp_f32_e32 v182, v182
	v_exp_f32_e32 v183, v183
	v_exp_f32_e32 v184, v184
	v_mfma_f32_16x16x32_f16 v[202:205], v[230:233], v[210:213], v[202:205]
	ds_read_b128 v[230:233], v255 offset:7168
	v_exp_f32_e32 v185, v185
	v_exp_f32_e32 v186, v186
	v_exp_f32_e32 v187, v187
	v_exp_f32_e32 v188, v188
	s_waitcnt lgkmcnt(5)
	ds_read_b128 v[210:213], v242 offset:27760
	v_mfma_f32_16x16x32_f16 v[190:193], v[18:21], v[214:217], v[190:193]
	v_exp_f32_e32 v189, v189
	v_add_f32_e32 v182, 1.0, v182
	v_add_f32_e32 v183, 1.0, v183
	v_add_f32_e32 v184, 1.0, v184
	v_mfma_f32_16x16x32_f16 v[194:197], v[22:25], v[214:217], v[194:197]
	v_add_f32_e32 v185, 1.0, v185
	v_add_f32_e32 v178, 1.0, v178
	v_add_f32_e32 v179, 1.0, v179
	v_add_f32_e32 v180, 1.0, v180
	v_mfma_f32_16x16x32_f16 v[198:201], v[26:29], v[214:217], v[198:201]
	v_add_f32_e32 v181, 1.0, v181
	v_fma_f32 v174, v174, v182, v182
	v_fma_f32 v175, v175, v183, v183
	v_fma_f32 v176, v176, v184, v184
	v_mfma_f32_16x16x32_f16 v[202:205], v[30:33], v[214:217], v[202:205]
	v_fma_f32 v177, v177, v185, v185
	v_rcp_f32_e32 v178, v178
	v_rcp_f32_e32 v179, v179
	v_rcp_f32_e32 v180, v180
	s_waitcnt lgkmcnt(5)
	ds_read_b128 v[214:217], v242 offset:27696
	v_mfma_f32_16x16x32_f16 v[190:193], v[34:37], v[206:209], v[190:193]
	v_rcp_f32_e32 v181, v181
	v_fma_f32 v182, v182, v252, s16
	v_fma_f32 v183, v183, v252, s16
	v_fma_f32 v184, v184, v252, s16
	v_mfma_f32_16x16x32_f16 v[194:197], v[38:41], v[206:209], v[194:197]
	v_fma_f32 v185, v185, v252, s16
	v_rcp_f32_e32 v174, v174
	v_rcp_f32_e32 v175, v175
	v_rcp_f32_e32 v176, v176
	v_mfma_f32_16x16x32_f16 v[198:201], v[42:45], v[206:209], v[198:201]
	v_rcp_f32_e32 v177, v177
	v_mul_f32_e32 v170, v170, v178
	v_mul_f32_e32 v171, v171, v179
	v_mul_f32_e32 v172, v172, v180
	v_mfma_f32_16x16x32_f16 v[202:205], v[46:49], v[206:209], v[202:205]
	v_mul_f32_e32 v173, v173, v181
	v_fma_f32 v170, v182, v174, v170
	v_fma_f32 v171, v183, v175, v171
	v_fma_f32 v172, v184, v176, v172
	s_waitcnt lgkmcnt(1)
	ds_read_b128 v[206:209], v242 offset:27712
	v_mfma_f32_16x16x32_f16 v[190:193], v[218:221], v[210:213], v[190:193]
	ds_read_b128 v[218:221], v255 offset:0
	v_fma_f32 v173, v185, v177, v173
	v_exp_f32_e32 v178, v170
	v_exp_f32_e32 v179, v171
	v_exp_f32_e32 v180, v172
	v_mfma_f32_16x16x32_f16 v[194:197], v[222:225], v[210:213], v[194:197]
	ds_read_b128 v[222:225], v255 offset:1024
	v_exp_f32_e32 v181, v173
	v_add_f32_e32 v174, 1.0, v178
	v_add_f32_e32 v175, 1.0, v179
	v_add_f32_e32 v176, 1.0, v180
	v_mfma_f32_16x16x32_f16 v[198:201], v[226:229], v[210:213], v[198:201]
	ds_read_b128 v[226:229], v255 offset:2048
	v_add_f32_e32 v177, 1.0, v181
	v_add_f32_e32 v182, -1.0, v178
	v_add_f32_e32 v183, -1.0, v179
	v_add_f32_e32 v184, -1.0, v180
	v_mfma_f32_16x16x32_f16 v[202:205], v[230:233], v[210:213], v[202:205]
	ds_read_b128 v[230:233], v255 offset:3072
	v_add_f32_e32 v185, -1.0, v181
	v_fma_f32 v186, v186, v174, v174
	v_fma_f32 v187, v187, v175, v175
	v_fma_f32 v188, v188, v176, v176
	s_waitcnt lgkmcnt(5)
	ds_read_b128 v[210:213], v242 offset:27728
	v_mfma_f32_16x16x32_f16 v[190:193], v[50:53], v[214:217], v[190:193]
	v_fma_f32 v189, v189, v177, v177
	v_rcp_f32_e32 v186, v186
	v_rcp_f32_e32 v187, v187
	v_rcp_f32_e32 v188, v188
	v_mfma_f32_16x16x32_f16 v[194:197], v[54:57], v[214:217], v[194:197]
	v_rcp_f32_e32 v189, v189
	v_mul_f32_e32 v186, v182, v186
	v_mul_f32_e32 v187, v183, v187
	v_mul_f32_e32 v188, v184, v188
	v_mfma_f32_16x16x32_f16 v[198:201], v[58:61], v[214:217], v[198:201]
	v_mul_f32_e32 v189, v185, v189
	v_cvt_pk_f16_f32 v186, v186, v187
	v_cvt_pk_f16_f32 v187, v188, v189
	ds_write_b64 v244, v[186:187] offset:17920
	v_mfma_f32_16x16x32_f16 v[202:205], v[62:65], v[214:217], v[202:205]
	ds_read_b128 v[174:177], v245 offset:0
	ds_read_b128 v[178:181], v245 offset:512
	ds_read_b128 v[182:185], v245 offset:1024
	ds_read_b128 v[186:189], v245 offset:1536
	s_waitcnt lgkmcnt(0)
	s_barrier
	ds_read_b128 v[234:237], v250 offset:15360
	s_mov_b64 exec, s[20:21]
	ds_read_b128 v[238:241], v250 offset:17920
	s_mov_b64 exec, -1
	ds_read_b128 v[214:217], v243 offset:15360
	v_mfma_f32_16x16x32_f16 v[190:193], v[66:69], v[206:209], v[190:193]
	v_mfma_f32_16x16x32_f16 v[194:197], v[70:73], v[206:209], v[194:197]
	v_mfma_f32_16x16x32_f16 v[198:201], v[74:77], v[206:209], v[198:201]
	v_mfma_f32_16x16x32_f16 v[202:205], v[78:81], v[206:209], v[202:205]
	ds_read_b128 v[206:209], v243 offset:15376
	v_mfma_f32_16x16x32_f16 v[190:193], v[82:85], v[210:213], v[190:193]
	v_mfma_f32_16x16x32_f16 v[194:197], v[86:89], v[210:213], v[194:197]
	v_mfma_f32_16x16x32_f16 v[198:201], v[90:93], v[210:213], v[198:201]
	v_mfma_f32_16x16x32_f16 v[202:205], v[94:97], v[210:213], v[202:205]
	s_waitcnt lgkmcnt(2)
	s_mov_b64 exec, s[18:19]
	global_store_dwordx4 v251, v[234:237], s[10:11]
	s_mov_b64 exec, s[20:21]
	global_store_dwordx4 v251, v[238:241], s[14:15]
	s_mov_b64 exec, -1
	s_add_u32 s10, s10, 0x271000
	s_addc_u32 s11, s11, 0
	s_add_u32 s14, s14, 0x271000
	s_addc_u32 s15, s15, 0
	s_waitcnt lgkmcnt(1)
	ds_read_b128 v[210:213], v243 offset:15392
	v_mfma_f32_16x16x32_f16 v[190:193], v[98:101], v[214:217], v[190:193]
	v_mfma_f32_16x16x32_f16 v[194:197], v[102:105], v[214:217], v[194:197]
	v_mfma_f32_16x16x32_f16 v[198:201], v[106:109], v[214:217], v[198:201]
	v_mfma_f32_16x16x32_f16 v[202:205], v[110:113], v[214:217], v[202:205]
	global_load_dwordx4 v[234:237], v246, s[12:13]
	s_waitcnt lgkmcnt(1)
	ds_read_b128 v[214:217], v243 offset:15408
	v_mfma_f32_16x16x32_f16 v[190:193], v[114:117], v[206:209], v[190:193]
	v_mfma_f32_16x16x32_f16 v[194:197], v[118:121], v[206:209], v[194:197]
	v_mfma_f32_16x16x32_f16 v[198:201], v[122:125], v[206:209], v[198:201]
	v_mfma_f32_16x16x32_f16 v[202:205], v[126:129], v[206:209], v[202:205]
	global_load_dwordx4 v[238:241], v247, s[8:9]
	s_waitcnt lgkmcnt(1)
	ds_read_b128 v[206:209], v242 offset:29952
	v_mfma_f32_16x16x32_f16 v[190:193], v[130:133], v[210:213], v[190:193]
	v_mfma_f32_16x16x32_f16 v[194:197], v[134:137], v[210:213], v[194:197]
	v_mfma_f32_16x16x32_f16 v[198:201], v[138:141], v[210:213], v[198:201]
	v_mfma_f32_16x16x32_f16 v[202:205], v[142:145], v[210:213], v[202:205]
	s_add_u32 s12, s12, 0x271000
	s_waitcnt lgkmcnt(1)
	ds_read_b128 v[210:213], v242 offset:29968
	v_mfma_f32_16x16x32_f16 v[190:193], v[146:149], v[214:217], v[190:193]
	v_mfma_f32_16x16x32_f16 v[194:197], v[150:153], v[214:217], v[194:197]
	v_mfma_f32_16x16x32_f16 v[198:201], v[154:157], v[214:217], v[198:201]
	v_mfma_f32_16x16x32_f16 v[202:205], v[158:161], v[214:217], v[202:205]
	s_addc_u32 s13, s13, 0
	s_waitcnt lgkmcnt(1)
	ds_read_b128 v[214:217], v242 offset:30048
	v_mfma_f32_16x16x32_f16 v[174:177], v[2:5], v[206:209], v[174:177]
	v_mfma_f32_16x16x32_f16 v[178:181], v[6:9], v[206:209], v[178:181]
	v_mfma_f32_16x16x32_f16 v[182:185], v[10:13], v[206:209], v[182:185]
	v_mfma_f32_16x16x32_f16 v[186:189], v[14:17], v[206:209], v[186:189]
	s_waitcnt lgkmcnt(1)
	ds_read_b128 v[206:209], v242 offset:29984
	v_mfma_f32_16x16x32_f16 v[174:177], v[18:21], v[210:213], v[174:177]
	v_mfma_f32_16x16x32_f16 v[178:181], v[22:25], v[210:213], v[178:181]
	v_mfma_f32_16x16x32_f16 v[182:185], v[26:29], v[210:213], v[182:185]
	v_mfma_f32_16x16x32_f16 v[186:189], v[30:33], v[210:213], v[186:189]
	s_waitcnt lgkmcnt(1)
	ds_read_b128 v[210:213], v242 offset:30000
	v_mfma_f32_16x16x32_f16 v[174:177], v[218:221], v[214:217], v[174:177]
	ds_read_b128 v[218:221], v255 offset:4096
	v_exp_f32_e32 v190, v190
	v_exp_f32_e32 v191, v191
	v_mfma_f32_16x16x32_f16 v[178:181], v[222:225], v[214:217], v[178:181]
	ds_read_b128 v[222:225], v255 offset:5120
	v_exp_f32_e32 v192, v192
	v_exp_f32_e32 v193, v193
	v_mfma_f32_16x16x32_f16 v[182:185], v[226:229], v[214:217], v[182:185]
	ds_read_b128 v[226:229], v255 offset:6144
	v_exp_f32_e32 v194, v194
	v_exp_f32_e32 v195, v195
	v_mfma_f32_16x16x32_f16 v[186:189], v[230:233], v[214:217], v[186:189]
	ds_read_b128 v[230:233], v255 offset:7168
	v_exp_f32_e32 v196, v196
	v_exp_f32_e32 v197, v197
	s_waitcnt lgkmcnt(5)
	ds_read_b128 v[214:217], v243 offset:16640
	v_mfma_f32_16x16x32_f16 v[174:177], v[34:37], v[206:209], v[174:177]
	v_exp_f32_e32 v198, v198
	v_exp_f32_e32 v199, v199
	v_mfma_f32_16x16x32_f16 v[178:181], v[38:41], v[206:209], v[178:181]
	v_exp_f32_e32 v200, v200
	v_exp_f32_e32 v201, v201
	v_mfma_f32_16x16x32_f16 v[182:185], v[42:45], v[206:209], v[182:185]
	v_exp_f32_e32 v202, v202
	v_exp_f32_e32 v203, v203
	v_mfma_f32_16x16x32_f16 v[186:189], v[46:49], v[206:209], v[186:189]
	v_exp_f32_e32 v204, v204
	v_exp_f32_e32 v205, v205
	v_add_f32_e32 v198, 1.0, v198
	s_waitcnt lgkmcnt(5)
	ds_read_b128 v[206:209], v243 offset:16656
	v_mfma_f32_16x16x32_f16 v[174:177], v[50:53], v[210:213], v[174:177]
	v_add_f32_e32 v199, 1.0, v199
	v_add_f32_e32 v200, 1.0, v200
	v_mfma_f32_16x16x32_f16 v[178:181], v[54:57], v[210:213], v[178:181]
	v_add_f32_e32 v201, 1.0, v201
	v_add_f32_e32 v194, 1.0, v194
	v_mfma_f32_16x16x32_f16 v[182:185], v[58:61], v[210:213], v[182:185]
	v_add_f32_e32 v195, 1.0, v195
	v_add_f32_e32 v196, 1.0, v196
	v_mfma_f32_16x16x32_f16 v[186:189], v[62:65], v[210:213], v[186:189]
	v_add_f32_e32 v197, 1.0, v197
	v_fma_f32 v190, v190, v198, v198
	v_fma_f32 v191, v191, v199, v199
	s_waitcnt lgkmcnt(1)
	ds_read_b128 v[210:213], v242 offset:30064
	v_mfma_f32_16x16x32_f16 v[174:177], v[98:101], v[214:217], v[174:177]
	v_fma_f32 v192, v192, v200, v200
	v_fma_f32 v193, v193, v201, v201
	v_mfma_f32_16x16x32_f16 v[178:181], v[102:105], v[214:217], v[178:181]
	v_rcp_f32_e32 v194, v194
	v_rcp_f32_e32 v195, v195
	v_mfma_f32_16x16x32_f16 v[182:185], v[106:109], v[214:217], v[182:185]
	v_rcp_f32_e32 v196, v196
	v_rcp_f32_e32 v197, v197
	v_mfma_f32_16x16x32_f16 v[186:189], v[110:113], v[214:217], v[186:189]
	v_fma_f32 v198, v198, v252, s16
	v_fma_f32 v199, v199, v252, s16
	v_fma_f32 v200, v200, v252, s16
	s_waitcnt lgkmcnt(1)
	ds_read_b128 v[214:217], v242 offset:30016
	v_mfma_f32_16x16x32_f16 v[174:177], v[114:117], v[206:209], v[174:177]
	v_fma_f32 v201, v201, v252, s16
	v_rcp_f32_e32 v190, v190
	v_mfma_f32_16x16x32_f16 v[178:181], v[118:121], v[206:209], v[178:181]
	v_rcp_f32_e32 v191, v191
	v_rcp_f32_e32 v192, v192
	v_mfma_f32_16x16x32_f16 v[182:185], v[122:125], v[206:209], v[182:185]
	v_rcp_f32_e32 v193, v193
	v_mul_f32_e32 v162, v162, v194
	v_mfma_f32_16x16x32_f16 v[186:189], v[126:129], v[206:209], v[186:189]
	v_mul_f32_e32 v163, v163, v195
	v_mul_f32_e32 v164, v164, v196
	s_waitcnt lgkmcnt(1)
	ds_read_b128 v[206:209], v242 offset:30032
	v_mfma_f32_16x16x32_f16 v[174:177], v[218:221], v[210:213], v[174:177]
	ds_read_b128 v[218:221], v255 offset:0
	v_mul_f32_e32 v165, v165, v197
	v_fma_f32 v162, v198, v190, v162
	v_mfma_f32_16x16x32_f16 v[178:181], v[222:225], v[210:213], v[178:181]
	ds_read_b128 v[222:225], v255 offset:1024
	v_fma_f32 v163, v199, v191, v163
	v_fma_f32 v164, v200, v192, v164
	v_mfma_f32_16x16x32_f16 v[182:185], v[226:229], v[210:213], v[182:185]
	ds_read_b128 v[226:229], v255 offset:2048
	v_fma_f32 v165, v201, v193, v165
	v_exp_f32_e32 v194, v162
	v_mfma_f32_16x16x32_f16 v[186:189], v[230:233], v[210:213], v[186:189]
	ds_read_b128 v[230:233], v255 offset:3072
	v_exp_f32_e32 v195, v163
	v_exp_f32_e32 v196, v164
	v_exp_f32_e32 v197, v165
	s_waitcnt lgkmcnt(5)
	ds_read_b128 v[210:213], v243 offset:16672
	v_mfma_f32_16x16x32_f16 v[174:177], v[66:69], v[214:217], v[174:177]
	v_add_f32_e32 v190, 1.0, v194
	v_add_f32_e32 v191, 1.0, v195
	v_mfma_f32_16x16x32_f16 v[178:181], v[70:73], v[214:217], v[178:181]
	v_add_f32_e32 v192, 1.0, v196
	v_add_f32_e32 v193, 1.0, v197
	v_mfma_f32_16x16x32_f16 v[182:185], v[74:77], v[214:217], v[182:185]
	v_add_f32_e32 v198, -1.0, v194
	v_add_f32_e32 v199, -1.0, v195
	v_mfma_f32_16x16x32_f16 v[186:189], v[78:81], v[214:217], v[186:189]
	v_add_f32_e32 v200, -1.0, v196
	v_add_f32_e32 v201, -1.0, v197
	v_fma_f32 v202, v202, v190, v190
	s_waitcnt lgkmcnt(5)
	ds_read_b128 v[214:217], v243 offset:16688
	v_mfma_f32_16x16x32_f16 v[174:177], v[82:85], v[206:209], v[174:177]
	s_waitcnt vmcnt(0)
	ds_write_b128 v249, v[234:237] offset:27648
	ds_write_b128 v249, v[238:241] offset:2304
	global_load_dwordx4 v[234:237], v248, s[8:9]
	s_add_u32 s8, s8, 0x271000
	s_addc_u32 s9, s9, 0
	v_fma_f32 v203, v203, v191, v191
	v_mfma_f32_16x16x32_f16 v[178:181], v[86:89], v[206:209], v[178:181]
	v_fma_f32 v204, v204, v192, v192
	v_fma_f32 v205, v205, v193, v193
	v_rcp_f32_e32 v202, v202
	v_mfma_f32_16x16x32_f16 v[182:185], v[90:93], v[206:209], v[182:185]
	v_rcp_f32_e32 v203, v203
	v_rcp_f32_e32 v204, v204
	v_mfma_f32_16x16x32_f16 v[186:189], v[94:97], v[206:209], v[186:189]
	v_rcp_f32_e32 v205, v205
	v_mul_f32_e32 v202, v198, v202
	v_mul_f32_e32 v203, v199, v203
	s_waitcnt lgkmcnt(3)
	ds_read_b128 v[206:209], v242 offset:32256
	v_mfma_f32_16x16x32_f16 v[174:177], v[130:133], v[210:213], v[174:177]
	v_mul_f32_e32 v204, v200, v204
	v_mul_f32_e32 v205, v201, v205
	v_mfma_f32_16x16x32_f16 v[178:181], v[134:137], v[210:213], v[178:181]
	v_cvt_pk_f16_f32 v202, v202, v203
	v_cvt_pk_f16_f32 v203, v204, v205
	v_mfma_f32_16x16x32_f16 v[182:185], v[138:141], v[210:213], v[182:185]
	ds_write_b64 v244, v[202:203] offset:0
	ds_read_b128 v[190:193], v245 offset:0
	v_mfma_f32_16x16x32_f16 v[186:189], v[142:145], v[210:213], v[186:189]
	ds_read_b128 v[194:197], v245 offset:512
	ds_read_b128 v[198:201], v245 offset:1024
	ds_read_b128 v[202:205], v245 offset:1536
	s_waitcnt lgkmcnt(8)
	ds_read_b128 v[210:213], v242 offset:32272
	v_mfma_f32_16x16x32_f16 v[174:177], v[146:149], v[214:217], v[174:177]
	v_mfma_f32_16x16x32_f16 v[178:181], v[150:153], v[214:217], v[178:181]
	v_mfma_f32_16x16x32_f16 v[182:185], v[154:157], v[214:217], v[182:185]
	v_mfma_f32_16x16x32_f16 v[186:189], v[158:161], v[214:217], v[186:189]
	s_waitcnt lgkmcnt(6)
	ds_read_b128 v[214:217], v242 offset:32352
	s_waitcnt lgkmcnt(5)
	v_mfma_f32_16x16x32_f16 v[190:193], v[2:5], v[206:209], v[190:193]
	s_waitcnt lgkmcnt(4)
	v_mfma_f32_16x16x32_f16 v[194:197], v[6:9], v[206:209], v[194:197]
	s_waitcnt lgkmcnt(3)
	v_mfma_f32_16x16x32_f16 v[198:201], v[10:13], v[206:209], v[198:201]
	s_waitcnt lgkmcnt(2)
	v_mfma_f32_16x16x32_f16 v[202:205], v[14:17], v[206:209], v[202:205]
	s_waitcnt lgkmcnt(1)
	ds_read_b128 v[206:209], v242 offset:32288
	v_mfma_f32_16x16x32_f16 v[190:193], v[18:21], v[210:213], v[190:193]
	v_mfma_f32_16x16x32_f16 v[194:197], v[22:25], v[210:213], v[194:197]
	v_mfma_f32_16x16x32_f16 v[198:201], v[26:29], v[210:213], v[198:201]
	v_mfma_f32_16x16x32_f16 v[202:205], v[30:33], v[210:213], v[202:205]
	s_waitcnt lgkmcnt(1)
	ds_read_b128 v[210:213], v242 offset:32304
	v_mfma_f32_16x16x32_f16 v[190:193], v[218:221], v[214:217], v[190:193]
	ds_read_b128 v[218:221], v255 offset:4096
	v_exp_f32_e32 v174, v174
	v_exp_f32_e32 v175, v175
	v_mfma_f32_16x16x32_f16 v[194:197], v[222:225], v[214:217], v[194:197]
	ds_read_b128 v[222:225], v255 offset:5120
	v_exp_f32_e32 v176, v176
	v_exp_f32_e32 v177, v177
	v_mfma_f32_16x16x32_f16 v[198:201], v[226:229], v[214:217], v[198:201]
	ds_read_b128 v[226:229], v255 offset:6144
	v_exp_f32_e32 v178, v178
	v_exp_f32_e32 v179, v179
	v_mfma_f32_16x16x32_f16 v[202:205], v[230:233], v[214:217], v[202:205]
	ds_read_b128 v[230:233], v255 offset:7168
	v_exp_f32_e32 v180, v180
	v_exp_f32_e32 v181, v181
	s_waitcnt lgkmcnt(5)
	ds_read_b128 v[214:217], v243 offset:17920
	v_mfma_f32_16x16x32_f16 v[190:193], v[34:37], v[206:209], v[190:193]
	v_exp_f32_e32 v182, v182
	v_exp_f32_e32 v183, v183
	v_mfma_f32_16x16x32_f16 v[194:197], v[38:41], v[206:209], v[194:197]
	v_exp_f32_e32 v184, v184
	v_exp_f32_e32 v185, v185
	v_mfma_f32_16x16x32_f16 v[198:201], v[42:45], v[206:209], v[198:201]
	v_exp_f32_e32 v186, v186
	v_exp_f32_e32 v187, v187
	v_mfma_f32_16x16x32_f16 v[202:205], v[46:49], v[206:209], v[202:205]
	v_exp_f32_e32 v188, v188
	v_exp_f32_e32 v189, v189
	v_add_f32_e32 v182, 1.0, v182
	s_waitcnt lgkmcnt(5)
	ds_read_b128 v[206:209], v243 offset:17936
	v_mfma_f32_16x16x32_f16 v[190:193], v[50:53], v[210:213], v[190:193]
	v_add_f32_e32 v183, 1.0, v183
	v_add_f32_e32 v184, 1.0, v184
	v_mfma_f32_16x16x32_f16 v[194:197], v[54:57], v[210:213], v[194:197]
	v_add_f32_e32 v185, 1.0, v185
	v_add_f32_e32 v178, 1.0, v178
	v_mfma_f32_16x16x32_f16 v[198:201], v[58:61], v[210:213], v[198:201]
	v_add_f32_e32 v179, 1.0, v179
	v_add_f32_e32 v180, 1.0, v180
	v_mfma_f32_16x16x32_f16 v[202:205], v[62:65], v[210:213], v[202:205]
	v_add_f32_e32 v181, 1.0, v181
	v_fma_f32 v174, v174, v182, v182
	v_fma_f32 v175, v175, v183, v183
	s_waitcnt lgkmcnt(1)
	ds_read_b128 v[210:213], v242 offset:32368
	v_mfma_f32_16x16x32_f16 v[190:193], v[98:101], v[214:217], v[190:193]
	v_fma_f32 v176, v176, v184, v184
	v_fma_f32 v177, v177, v185, v185
	v_mfma_f32_16x16x32_f16 v[194:197], v[102:105], v[214:217], v[194:197]
	v_rcp_f32_e32 v178, v178
	v_rcp_f32_e32 v179, v179
	v_mfma_f32_16x16x32_f16 v[198:201], v[106:109], v[214:217], v[198:201]
	v_rcp_f32_e32 v180, v180
	v_rcp_f32_e32 v181, v181
	v_mfma_f32_16x16x32_f16 v[202:205], v[110:113], v[214:217], v[202:205]
	v_fma_f32 v182, v182, v252, s16
	v_fma_f32 v183, v183, v252, s16
	v_fma_f32 v184, v184, v252, s16
	s_waitcnt lgkmcnt(1)
	ds_read_b128 v[214:217], v242 offset:32320
	v_mfma_f32_16x16x32_f16 v[190:193], v[114:117], v[206:209], v[190:193]
	v_fma_f32 v185, v185, v252, s16
	v_rcp_f32_e32 v174, v174
	v_mfma_f32_16x16x32_f16 v[194:197], v[118:121], v[206:209], v[194:197]
	v_rcp_f32_e32 v175, v175
	v_rcp_f32_e32 v176, v176
	v_mfma_f32_16x16x32_f16 v[198:201], v[122:125], v[206:209], v[198:201]
	v_rcp_f32_e32 v177, v177
	v_mul_f32_e32 v166, v166, v178
	v_mfma_f32_16x16x32_f16 v[202:205], v[126:129], v[206:209], v[202:205]
	v_mul_f32_e32 v167, v167, v179
	v_mul_f32_e32 v168, v168, v180
	s_waitcnt lgkmcnt(1)
	ds_read_b128 v[206:209], v242 offset:32336
	v_mfma_f32_16x16x32_f16 v[190:193], v[218:221], v[210:213], v[190:193]
	ds_read_b128 v[218:221], v255 offset:0
	v_mul_f32_e32 v169, v169, v181
	v_fma_f32 v166, v182, v174, v166
	v_mfma_f32_16x16x32_f16 v[194:197], v[222:225], v[210:213], v[194:197]
	ds_read_b128 v[222:225], v255 offset:1024
	v_fma_f32 v167, v183, v175, v167
	v_fma_f32 v168, v184, v176, v168
	v_mfma_f32_16x16x32_f16 v[198:201], v[226:229], v[210:213], v[198:201]
	ds_read_b128 v[226:229], v255 offset:2048
	v_fma_f32 v169, v185, v177, v169
	v_exp_f32_e32 v178, v166
	v_mfma_f32_16x16x32_f16 v[202:205], v[230:233], v[210:213], v[202:205]
	ds_read_b128 v[230:233], v255 offset:3072
	v_exp_f32_e32 v179, v167
	v_exp_f32_e32 v180, v168
	v_exp_f32_e32 v181, v169
	s_waitcnt lgkmcnt(5)
	ds_read_b128 v[210:213], v243 offset:17952
	v_mfma_f32_16x16x32_f16 v[190:193], v[66:69], v[214:217], v[190:193]
	v_add_f32_e32 v174, 1.0, v178
	v_add_f32_e32 v175, 1.0, v179
	v_mfma_f32_16x16x32_f16 v[194:197], v[70:73], v[214:217], v[194:197]
	v_add_f32_e32 v176, 1.0, v180
	v_add_f32_e32 v177, 1.0, v181
	v_mfma_f32_16x16x32_f16 v[198:201], v[74:77], v[214:217], v[198:201]
	v_add_f32_e32 v182, -1.0, v178
	v_add_f32_e32 v183, -1.0, v179
	v_mfma_f32_16x16x32_f16 v[202:205], v[78:81], v[214:217], v[202:205]
	v_add_f32_e32 v184, -1.0, v180
	v_add_f32_e32 v185, -1.0, v181
	v_fma_f32 v186, v186, v174, v174
	s_waitcnt lgkmcnt(5)
	ds_read_b128 v[214:217], v243 offset:17968
	v_mfma_f32_16x16x32_f16 v[190:193], v[82:85], v[206:209], v[190:193]
	v_fma_f32 v187, v187, v175, v175
	v_fma_f32 v188, v188, v176, v176
	v_mfma_f32_16x16x32_f16 v[194:197], v[86:89], v[206:209], v[194:197]
	v_fma_f32 v189, v189, v177, v177
	v_rcp_f32_e32 v186, v186
	v_mfma_f32_16x16x32_f16 v[198:201], v[90:93], v[206:209], v[198:201]
	v_rcp_f32_e32 v187, v187
	v_rcp_f32_e32 v188, v188
	v_mfma_f32_16x16x32_f16 v[202:205], v[94:97], v[206:209], v[202:205]
	v_rcp_f32_e32 v189, v189
	v_mul_f32_e32 v186, v182, v186
	v_mul_f32_e32 v187, v183, v187
	s_waitcnt lgkmcnt(1)
	ds_read_b128 v[206:209], v242 offset:0
	v_mfma_f32_16x16x32_f16 v[190:193], v[130:133], v[210:213], v[190:193]
	v_mul_f32_e32 v188, v184, v188
	v_mul_f32_e32 v189, v185, v189
	v_mfma_f32_16x16x32_f16 v[194:197], v[134:137], v[210:213], v[194:197]
	v_cvt_pk_f16_f32 v186, v186, v187
	v_cvt_pk_f16_f32 v187, v188, v189
	v_mfma_f32_16x16x32_f16 v[198:201], v[138:141], v[210:213], v[198:201]
	ds_write_b64 v244, v[186:187] offset:1280
	ds_read_b128 v[174:177], v245 offset:0
	v_mfma_f32_16x16x32_f16 v[202:205], v[142:145], v[210:213], v[202:205]
	ds_read_b128 v[178:181], v245 offset:512
	ds_read_b128 v[182:185], v245 offset:1024
	ds_read_b128 v[186:189], v245 offset:1536
	s_waitcnt lgkmcnt(6)
	ds_read_b128 v[210:213], v242 offset:96
	v_mfma_f32_16x16x32_f16 v[190:193], v[146:149], v[214:217], v[190:193]
	v_mfma_f32_16x16x32_f16 v[194:197], v[150:153], v[214:217], v[194:197]
	v_mfma_f32_16x16x32_f16 v[198:201], v[154:157], v[214:217], v[198:201]
	v_mfma_f32_16x16x32_f16 v[202:205], v[158:161], v[214:217], v[202:205]
	s_waitcnt vmcnt(0)
	ds_write_b128 v249, v[234:237] offset:4608
	s_waitcnt lgkmcnt(7)
	ds_read_b128 v[214:217], v242 offset:16
	s_waitcnt lgkmcnt(6)
	v_mfma_f32_16x16x32_f16 v[174:177], v[2:5], v[206:209], v[174:177]
	s_waitcnt lgkmcnt(5)
	v_mfma_f32_16x16x32_f16 v[178:181], v[6:9], v[206:209], v[178:181]
	s_waitcnt lgkmcnt(4)
	v_mfma_f32_16x16x32_f16 v[182:185], v[10:13], v[206:209], v[182:185]
	s_waitcnt lgkmcnt(3)
	v_mfma_f32_16x16x32_f16 v[186:189], v[14:17], v[206:209], v[186:189]
	s_waitcnt lgkmcnt(2)
	ds_read_b128 v[206:209], v242 offset:32
	v_mfma_f32_16x16x32_f16 v[174:177], v[218:221], v[210:213], v[174:177]
	ds_read_b128 v[218:221], v255 offset:4096
	v_exp_f32_e32 v190, v190
	v_exp_f32_e32 v191, v191
	v_exp_f32_e32 v192, v192
	v_mfma_f32_16x16x32_f16 v[178:181], v[222:225], v[210:213], v[178:181]
	ds_read_b128 v[222:225], v255 offset:5120
	v_exp_f32_e32 v193, v193
	v_exp_f32_e32 v194, v194
	v_exp_f32_e32 v195, v195
	v_exp_f32_e32 v196, v196
	v_mfma_f32_16x16x32_f16 v[182:185], v[226:229], v[210:213], v[182:185]
	ds_read_b128 v[226:229], v255 offset:6144
	v_exp_f32_e32 v197, v197
	v_exp_f32_e32 v198, v198
	v_exp_f32_e32 v199, v199
	v_exp_f32_e32 v200, v200
	v_mfma_f32_16x16x32_f16 v[186:189], v[230:233], v[210:213], v[186:189]
	ds_read_b128 v[230:233], v255 offset:7168
	v_exp_f32_e32 v201, v201
	v_exp_f32_e32 v202, v202
	v_exp_f32_e32 v203, v203
	v_exp_f32_e32 v204, v204
	s_waitcnt lgkmcnt(5)
	ds_read_b128 v[210:213], v242 offset:112
	v_mfma_f32_16x16x32_f16 v[174:177], v[18:21], v[214:217], v[174:177]
	v_exp_f32_e32 v205, v205
	v_add_f32_e32 v198, 1.0, v198
	v_add_f32_e32 v199, 1.0, v199
	v_add_f32_e32 v200, 1.0, v200
	v_mfma_f32_16x16x32_f16 v[178:181], v[22:25], v[214:217], v[178:181]
	v_add_f32_e32 v201, 1.0, v201
	v_add_f32_e32 v194, 1.0, v194
	v_add_f32_e32 v195, 1.0, v195
	v_add_f32_e32 v196, 1.0, v196
	v_mfma_f32_16x16x32_f16 v[182:185], v[26:29], v[214:217], v[182:185]
	v_add_f32_e32 v197, 1.0, v197
	v_fma_f32 v190, v190, v198, v198
	v_fma_f32 v191, v191, v199, v199
	v_fma_f32 v192, v192, v200, v200
	v_mfma_f32_16x16x32_f16 v[186:189], v[30:33], v[214:217], v[186:189]
	v_fma_f32 v193, v193, v201, v201
	v_rcp_f32_e32 v194, v194
	v_rcp_f32_e32 v195, v195
	v_rcp_f32_e32 v196, v196
	s_waitcnt lgkmcnt(5)
	ds_read_b128 v[214:217], v242 offset:48
	v_mfma_f32_16x16x32_f16 v[174:177], v[34:37], v[206:209], v[174:177]
	v_rcp_f32_e32 v197, v197
	v_fma_f32 v198, v198, v252, s16
	v_fma_f32 v199, v199, v252, s16
	v_fma_f32 v200, v200, v252, s16
	v_mfma_f32_16x16x32_f16 v[178:181], v[38:41], v[206:209], v[178:181]
	v_fma_f32 v201, v201, v252, s16
	v_rcp_f32_e32 v190, v190
	v_rcp_f32_e32 v191, v191
	v_rcp_f32_e32 v192, v192
	v_mfma_f32_16x16x32_f16 v[182:185], v[42:45], v[206:209], v[182:185]
	v_rcp_f32_e32 v193, v193
	v_mul_f32_e32 v170, v170, v194
	v_mul_f32_e32 v171, v171, v195
	v_mul_f32_e32 v172, v172, v196
	v_mfma_f32_16x16x32_f16 v[186:189], v[46:49], v[206:209], v[186:189]
	v_mul_f32_e32 v173, v173, v197
	v_fma_f32 v170, v198, v190, v170
	v_fma_f32 v171, v199, v191, v171
	v_fma_f32 v172, v200, v192, v172
	s_waitcnt lgkmcnt(1)
	ds_read_b128 v[206:209], v242 offset:64
	v_mfma_f32_16x16x32_f16 v[174:177], v[218:221], v[210:213], v[174:177]
	ds_read_b128 v[218:221], v255 offset:0
	v_fma_f32 v173, v201, v193, v173
	v_exp_f32_e32 v194, v170
	v_exp_f32_e32 v195, v171
	v_exp_f32_e32 v196, v172
	v_mfma_f32_16x16x32_f16 v[178:181], v[222:225], v[210:213], v[178:181]
	ds_read_b128 v[222:225], v255 offset:1024
	v_exp_f32_e32 v197, v173
	v_add_f32_e32 v190, 1.0, v194
	v_add_f32_e32 v191, 1.0, v195
	v_add_f32_e32 v192, 1.0, v196
	v_mfma_f32_16x16x32_f16 v[182:185], v[226:229], v[210:213], v[182:185]
	ds_read_b128 v[226:229], v255 offset:2048
	v_add_f32_e32 v193, 1.0, v197
	v_add_f32_e32 v198, -1.0, v194
	v_add_f32_e32 v199, -1.0, v195
	v_add_f32_e32 v200, -1.0, v196
	v_mfma_f32_16x16x32_f16 v[186:189], v[230:233], v[210:213], v[186:189]
	ds_read_b128 v[230:233], v255 offset:3072
	v_add_f32_e32 v201, -1.0, v197
	v_fma_f32 v202, v202, v190, v190
	v_fma_f32 v203, v203, v191, v191
	v_fma_f32 v204, v204, v192, v192
	s_waitcnt lgkmcnt(5)
	ds_read_b128 v[210:213], v242 offset:80
	v_mfma_f32_16x16x32_f16 v[174:177], v[50:53], v[214:217], v[174:177]
	v_fma_f32 v205, v205, v193, v193
	v_rcp_f32_e32 v202, v202
	v_rcp_f32_e32 v203, v203
	v_rcp_f32_e32 v204, v204
	v_mfma_f32_16x16x32_f16 v[178:181], v[54:57], v[214:217], v[178:181]
	v_rcp_f32_e32 v205, v205
	v_mul_f32_e32 v202, v198, v202
	v_mul_f32_e32 v203, v199, v203
	v_mul_f32_e32 v204, v200, v204
	v_mfma_f32_16x16x32_f16 v[182:185], v[58:61], v[214:217], v[182:185]
	v_mul_f32_e32 v205, v201, v205
	v_cvt_pk_f16_f32 v202, v202, v203
	v_cvt_pk_f16_f32 v203, v204, v205
	ds_write_b64 v244, v[202:203] offset:2560
	v_mfma_f32_16x16x32_f16 v[186:189], v[62:65], v[214:217], v[186:189]
	ds_read_b128 v[190:193], v245 offset:0
	ds_read_b128 v[194:197], v245 offset:512
	ds_read_b128 v[198:201], v245 offset:1024
	ds_read_b128 v[202:205], v245 offset:1536
	s_waitcnt lgkmcnt(0)
	s_barrier
	s_add_u32 s17, s17, 2
	s_cmp_lt_u32 s17, 16
	s_cbranch_scc1 .Llstm1_loop
	s_waitcnt lgkmcnt(0)
	ds_read_b128 v[234:237], v250
	s_mov_b64 exec, s[20:21]
	ds_read_b128 v[238:241], v250 offset:2560
	s_mov_b64 exec, -1
	s_waitcnt lgkmcnt(0)
	s_mov_b64 exec, s[18:19]
	global_store_dwordx4 v251, v[234:237], s[10:11]
	s_mov_b64 exec, s[20:21]
	global_store_dwordx4 v251, v[238:241], s[14:15]
	s_mov_b64 exec, -1
	s_branch .LBB6_39

.Lskipx51:
	s_waitcnt lgkmcnt(1)
	ds_read_b128 v[174:177], v195 offset:32
	v_mfma_f32_16x16x32_f16 v[142:145], v[66:69], v[178:181], v[142:145]
	v_mfma_f32_16x16x32_f16 v[146:149], v[70:73], v[178:181], v[146:149]
	v_mfma_f32_16x16x32_f16 v[150:153], v[74:77], v[178:181], v[150:153]
	v_mfma_f32_16x16x32_f16 v[154:157], v[78:81], v[178:181], v[154:157]
	global_load_dwordx4 v[190:193], v199, s[8:9]
	s_waitcnt lgkmcnt(1)
	ds_read_b128 v[178:181], v195 offset:48
	v_mfma_f32_16x16x32_f16 v[142:145], v[82:85], v[182:185], v[142:145]
	v_mfma_f32_16x16x32_f16 v[146:149], v[86:89], v[182:185], v[146:149]
	v_mfma_f32_16x16x32_f16 v[150:153], v[90:93], v[182:185], v[150:153]
	v_mfma_f32_16x16x32_f16 v[154:157], v[94:97], v[182:185], v[154:157]
	s_add_u32 s12, s12, 0x271000
	s_waitcnt lgkmcnt(1)
	ds_read_b128 v[182:185], v194 offset:1280
	v_mfma_f32_16x16x32_f16 v[142:145], v[98:101], v[174:177], v[142:145]
	v_mfma_f32_16x16x32_f16 v[146:149], v[102:105], v[174:177], v[146:149]
	v_mfma_f32_16x16x32_f16 v[150:153], v[106:109], v[174:177], v[150:153]
	v_mfma_f32_16x16x32_f16 v[154:157], v[110:113], v[174:177], v[154:157]
	s_addc_u32 s13, s13, 0
	s_waitcnt lgkmcnt(1)
	ds_read_b128 v[174:177], v194 offset:1296
	v_mfma_f32_16x16x32_f16 v[142:145], v[114:117], v[178:181], v[142:145]
	v_mfma_f32_16x16x32_f16 v[146:149], v[118:121], v[178:181], v[146:149]
	s_add_u32 s8, s8, 0x271000
	v_mfma_f32_16x16x32_f16 v[150:153], v[122:125], v[178:181], v[150:153]
	v_mfma_f32_16x16x32_f16 v[154:157], v[126:129], v[178:181], v[154:157]
	s_addc_u32 s9, s9, 0
	s_waitcnt lgkmcnt(1)
	ds_read_b128 v[178:181], v195 offset:1280
	v_mfma_f32_16x16x32_f16 v[158:161], v[2:5], v[182:185], v[158:161]
	v_mfma_f32_16x16x32_f16 v[162:165], v[6:9], v[182:185], v[162:165]
	v_mfma_f32_16x16x32_f16 v[166:169], v[10:13], v[182:185], v[166:169]
	v_mfma_f32_16x16x32_f16 v[170:173], v[14:17], v[182:185], v[170:173]
	s_waitcnt lgkmcnt(1)
	ds_read_b128 v[182:185], v195 offset:1296
	v_mfma_f32_16x16x32_f16 v[158:161], v[18:21], v[174:177], v[158:161]
	v_mfma_f32_16x16x32_f16 v[162:165], v[22:25], v[174:177], v[162:165]
	v_mfma_f32_16x16x32_f16 v[166:169], v[26:29], v[174:177], v[166:169]
	v_mfma_f32_16x16x32_f16 v[170:173], v[30:33], v[174:177], v[170:173]
	s_waitcnt lgkmcnt(1)
	ds_read_b128 v[174:177], v194 offset:1312
	v_mfma_f32_16x16x32_f16 v[158:161], v[66:69], v[178:181], v[158:161]
	v_exp_f32_e32 v142, v142
	v_exp_f32_e32 v143, v143
	v_exp_f32_e32 v144, v144
	v_mfma_f32_16x16x32_f16 v[162:165], v[70:73], v[178:181], v[162:165]
	v_exp_f32_e32 v145, v145
	v_exp_f32_e32 v146, v146
	v_exp_f32_e32 v147, v147
	v_exp_f32_e32 v148, v148
	v_mfma_f32_16x16x32_f16 v[166:169], v[74:77], v[178:181], v[166:169]
	v_exp_f32_e32 v149, v149
	v_exp_f32_e32 v150, v150
	v_exp_f32_e32 v151, v151
	v_exp_f32_e32 v152, v152
	v_mfma_f32_16x16x32_f16 v[170:173], v[78:81], v[178:181], v[170:173]
	v_exp_f32_e32 v153, v153
	v_exp_f32_e32 v154, v154
	v_exp_f32_e32 v155, v155
	v_exp_f32_e32 v156, v156
	s_waitcnt lgkmcnt(1)
	ds_read_b128 v[178:181], v194 offset:1328
	v_mfma_f32_16x16x32_f16 v[158:161], v[82:85], v[182:185], v[158:161]
	v_exp_f32_e32 v157, v157
	v_add_f32_e32 v150, 1.0, v150
	v_add_f32_e32 v151, 1.0, v151
	v_add_f32_e32 v152, 1.0, v152
	v_mfma_f32_16x16x32_f16 v[162:165], v[86:89], v[182:185], v[162:165]
	v_add_f32_e32 v153, 1.0, v153
	v_add_f32_e32 v146, 1.0, v146
	v_add_f32_e32 v147, 1.0, v147
	v_add_f32_e32 v148, 1.0, v148
	v_mfma_f32_16x16x32_f16 v[166:169], v[90:93], v[182:185], v[166:169]
	v_add_f32_e32 v149, 1.0, v149
	v_fma_f32 v142, v142, v150, v150
	v_fma_f32 v143, v143, v151, v151
	v_fma_f32 v144, v144, v152, v152
	v_mfma_f32_16x16x32_f16 v[170:173], v[94:97], v[182:185], v[170:173]
	v_fma_f32 v145, v145, v153, v153
	v_rcp_f32_e32 v146, v146
	v_rcp_f32_e32 v147, v147
	v_rcp_f32_e32 v148, v148
	s_waitcnt lgkmcnt(1)
	ds_read_b128 v[182:185], v195 offset:1312
	v_mfma_f32_16x16x32_f16 v[158:161], v[34:37], v[174:177], v[158:161]
	v_rcp_f32_e32 v149, v149
	v_fma_f32 v150, v150, v204, s16
	v_fma_f32 v151, v151, v204, s16
	v_fma_f32 v152, v152, v204, s16
	v_mfma_f32_16x16x32_f16 v[162:165], v[38:41], v[174:177], v[162:165]
	v_fma_f32 v153, v153, v204, s16
	v_rcp_f32_e32 v142, v142
	v_rcp_f32_e32 v143, v143
	v_rcp_f32_e32 v144, v144
	v_mfma_f32_16x16x32_f16 v[166:169], v[42:45], v[174:177], v[166:169]
	v_rcp_f32_e32 v145, v145
	v_mul_f32_e32 v130, v130, v146
	v_mul_f32_e32 v131, v131, v147
	v_mul_f32_e32 v132, v132, v148
	v_mfma_f32_16x16x32_f16 v[170:173], v[46:49], v[174:177], v[170:173]
	v_mul_f32_e32 v133, v133, v149
	v_fma_f32 v130, v150, v142, v130
	v_fma_f32 v131, v151, v143, v131
	v_fma_f32 v132, v152, v144, v132
	s_waitcnt lgkmcnt(1)
	ds_read_b128 v[174:177], v195 offset:1328
	v_mfma_f32_16x16x32_f16 v[158:161], v[50:53], v[178:181], v[158:161]
	s_waitcnt vmcnt(0)
	s_cmp_ge_u32 s24, 4
	s_cbranch_scc1 .Lskips52
	ds_write_b128 v201, v[186:189] offset:0
.Lskips52:
	ds_write_b128 v201, v[190:193] offset:16640
	v_fma_f32 v133, v153, v145, v133
	v_exp_f32_e32 v146, v130
	v_exp_f32_e32 v147, v131
	v_mfma_f32_16x16x32_f16 v[162:165], v[54:57], v[178:181], v[162:165]
	v_exp_f32_e32 v148, v132
	v_exp_f32_e32 v149, v133
	v_add_f32_e32 v142, 1.0, v146
	v_add_f32_e32 v143, 1.0, v147
	v_mfma_f32_16x16x32_f16 v[166:169], v[58:61], v[178:181], v[166:169]
	v_add_f32_e32 v144, 1.0, v148
	v_add_f32_e32 v145, 1.0, v149
	v_add_f32_e32 v150, -1.0, v146
	v_add_f32_e32 v151, -1.0, v147
	v_mfma_f32_16x16x32_f16 v[170:173], v[62:65], v[178:181], v[170:173]
	v_add_f32_e32 v152, -1.0, v148
	v_add_f32_e32 v153, -1.0, v149
	v_fma_f32 v154, v154, v142, v142
	v_fma_f32 v155, v155, v143, v143
	v_fma_f32 v156, v156, v144, v144
	s_waitcnt lgkmcnt(3)
	ds_read_b128 v[178:181], v194 offset:2560
	v_mfma_f32_16x16x32_f16 v[158:161], v[98:101], v[182:185], v[158:161]
	v_fma_f32 v157, v157, v145, v145
	v_rcp_f32_e32 v154, v154
	v_rcp_f32_e32 v155, v155
	v_rcp_f32_e32 v156, v156
	v_mfma_f32_16x16x32_f16 v[162:165], v[102:105], v[182:185], v[162:165]
	v_rcp_f32_e32 v157, v157
	v_mul_f32_e32 v154, v150, v154
	v_mul_f32_e32 v155, v151, v155
	v_mul_f32_e32 v156, v152, v156
	v_mfma_f32_16x16x32_f16 v[166:169], v[106:109], v[182:185], v[166:169]
	v_mul_f32_e32 v157, v153, v157
	v_cvt_pk_f16_f32 v154, v154, v155
	v_cvt_pk_f16_f32 v155, v156, v157
	ds_write_b64 v196, v[154:155] offset:15360
	v_mfma_f32_16x16x32_f16 v[170:173], v[110:113], v[182:185], v[170:173]
	ds_read_b128 v[142:145], v197 offset:0
	ds_read_b128 v[146:149], v197 offset:512
	ds_read_b128 v[150:153], v197 offset:1024
	ds_read_b128 v[154:157], v197 offset:1536
	s_waitcnt lgkmcnt(8)
	ds_read_b128 v[182:185], v194 offset:2576
	v_mfma_f32_16x16x32_f16 v[158:161], v[114:117], v[174:177], v[158:161]
	v_mfma_f32_16x16x32_f16 v[162:165], v[118:121], v[174:177], v[162:165]
	v_mfma_f32_16x16x32_f16 v[166:169], v[122:125], v[174:177], v[166:169]
	v_mfma_f32_16x16x32_f16 v[170:173], v[126:129], v[174:177], v[170:173]
	s_waitcnt lgkmcnt(6)
	ds_read_b128 v[174:177], v195 offset:2560
	s_waitcnt lgkmcnt(5)
	v_mfma_f32_16x16x32_f16 v[142:145], v[2:5], v[178:181], v[142:145]
	s_waitcnt lgkmcnt(4)
	v_mfma_f32_16x16x32_f16 v[146:149], v[6:9], v[178:181], v[146:149]
	s_waitcnt lgkmcnt(3)
	v_mfma_f32_16x16x32_f16 v[150:153], v[10:13], v[178:181], v[150:153]
	s_waitcnt lgkmcnt(2)
	v_mfma_f32_16x16x32_f16 v[154:157], v[14:17], v[178:181], v[154:157]
	s_waitcnt lgkmcnt(1)
	ds_read_b128 v[178:181], v195 offset:2576
	v_mfma_f32_16x16x32_f16 v[142:145], v[18:21], v[182:185], v[142:145]
	v_mfma_f32_16x16x32_f16 v[146:149], v[22:25], v[182:185], v[146:149]
	v_mfma_f32_16x16x32_f16 v[150:153], v[26:29], v[182:185], v[150:153]
	v_mfma_f32_16x16x32_f16 v[154:157], v[30:33], v[182:185], v[154:157]
	s_waitcnt lgkmcnt(1)
	ds_read_b128 v[182:185], v194 offset:2592
	v_mfma_f32_16x16x32_f16 v[142:145], v[66:69], v[174:177], v[142:145]
	v_exp_f32_e32 v158, v158
	v_exp_f32_e32 v159, v159
	v_exp_f32_e32 v160, v160
	v_mfma_f32_16x16x32_f16 v[146:149], v[70:73], v[174:177], v[146:149]
	v_exp_f32_e32 v161, v161
	v_exp_f32_e32 v162, v162
	v_exp_f32_e32 v163, v163
	v_exp_f32_e32 v164, v164
	v_mfma_f32_16x16x32_f16 v[150:153], v[74:77], v[174:177], v[150:153]
	v_exp_f32_e32 v165, v165
	v_exp_f32_e32 v166, v166
	v_exp_f32_e32 v167, v167
	v_exp_f32_e32 v168, v168
	v_mfma_f32_16x16x32_f16 v[154:157], v[78:81], v[174:177], v[154:157]
	v_exp_f32_e32 v169, v169
	v_exp_f32_e32 v170, v170
	v_exp_f32_e32 v171, v171
	v_exp_f32_e32 v172, v172
	s_waitcnt lgkmcnt(1)
	ds_read_b128 v[174:177], v194 offset:2608
	v_mfma_f32_16x16x32_f16 v[142:145], v[82:85], v[178:181], v[142:145]
	v_exp_f32_e32 v173, v173
	v_add_f32_e32 v166, 1.0, v166
	v_add_f32_e32 v167, 1.0, v167
	v_add_f32_e32 v168, 1.0, v168
	v_mfma_f32_16x16x32_f16 v[146:149], v[86:89], v[178:181], v[146:149]
	v_add_f32_e32 v169, 1.0, v169
	v_add_f32_e32 v162, 1.0, v162
	v_add_f32_e32 v163, 1.0, v163
	v_add_f32_e32 v164, 1.0, v164
	v_mfma_f32_16x16x32_f16 v[150:153], v[90:93], v[178:181], v[150:153]
	v_add_f32_e32 v165, 1.0, v165
	v_fma_f32 v158, v158, v166, v166
	v_fma_f32 v159, v159, v167, v167
	v_fma_f32 v160, v160, v168, v168
	v_mfma_f32_16x16x32_f16 v[154:157], v[94:97], v[178:181], v[154:157]
	v_fma_f32 v161, v161, v169, v169
	v_rcp_f32_e32 v162, v162
	v_rcp_f32_e32 v163, v163
	v_rcp_f32_e32 v164, v164
	s_waitcnt lgkmcnt(1)
	ds_read_b128 v[178:181], v195 offset:2592
	v_mfma_f32_16x16x32_f16 v[142:145], v[34:37], v[182:185], v[142:145]
	v_rcp_f32_e32 v165, v165
	v_fma_f32 v166, v166, v204, s16
	v_fma_f32 v167, v167, v204, s16
	v_fma_f32 v168, v168, v204, s16
	v_mfma_f32_16x16x32_f16 v[146:149], v[38:41], v[182:185], v[146:149]
	v_fma_f32 v169, v169, v204, s16
	v_rcp_f32_e32 v158, v158
	v_rcp_f32_e32 v159, v159
	v_rcp_f32_e32 v160, v160
	v_mfma_f32_16x16x32_f16 v[150:153], v[42:45], v[182:185], v[150:153]
	v_rcp_f32_e32 v161, v161
	v_mul_f32_e32 v134, v134, v162
	v_mul_f32_e32 v135, v135, v163
	v_mul_f32_e32 v136, v136, v164
	v_mfma_f32_16x16x32_f16 v[154:157], v[46:49], v[182:185], v[154:157]
	v_mul_f32_e32 v137, v137, v165
	v_fma_f32 v134, v166, v158, v134
	v_fma_f32 v135, v167, v159, v135
	v_fma_f32 v136, v168, v160, v136
	s_waitcnt lgkmcnt(1)
	ds_read_b128 v[182:185], v195 offset:2608
	v_mfma_f32_16x16x32_f16 v[142:145], v[50:53], v[174:177], v[142:145]
	v_fma_f32 v137, v169, v161, v137
	v_exp_f32_e32 v162, v134
	v_exp_f32_e32 v163, v135
	v_exp_f32_e32 v164, v136
	v_mfma_f32_16x16x32_f16 v[146:149], v[54:57], v[174:177], v[146:149]
	v_exp_f32_e32 v165, v137
	v_add_f32_e32 v158, 1.0, v162
	v_add_f32_e32 v159, 1.0, v163
	v_add_f32_e32 v160, 1.0, v164
	v_mfma_f32_16x16x32_f16 v[150:153], v[58:61], v[174:177], v[150:153]
	v_add_f32_e32 v161, 1.0, v165
	v_add_f32_e32 v166, -1.0, v162
	v_add_f32_e32 v167, -1.0, v163
	v_add_f32_e32 v168, -1.0, v164
	v_mfma_f32_16x16x32_f16 v[154:157], v[62:65], v[174:177], v[154:157]
	v_add_f32_e32 v169, -1.0, v165
	v_fma_f32 v170, v170, v158, v158
	v_fma_f32 v171, v171, v159, v159
	v_fma_f32 v172, v172, v160, v160
	s_waitcnt lgkmcnt(1)
	ds_read_b128 v[174:177], v194 offset:15360
	v_mfma_f32_16x16x32_f16 v[142:145], v[98:101], v[178:181], v[142:145]
	v_fma_f32 v173, v173, v161, v161
	v_rcp_f32_e32 v170, v170
	v_rcp_f32_e32 v171, v171
	v_rcp_f32_e32 v172, v172
	v_mfma_f32_16x16x32_f16 v[146:149], v[102:105], v[178:181], v[146:149]
	v_rcp_f32_e32 v173, v173
	v_mul_f32_e32 v170, v166, v170
	v_mul_f32_e32 v171, v167, v171
	v_mul_f32_e32 v172, v168, v172
	v_mfma_f32_16x16x32_f16 v[150:153], v[106:109], v[178:181], v[150:153]
	v_mul_f32_e32 v173, v169, v173
	v_cvt_pk_f16_f32 v170, v170, v171
	v_cvt_pk_f16_f32 v171, v172, v173
	ds_write_b64 v196, v[170:171] offset:16640
	v_mfma_f32_16x16x32_f16 v[154:157], v[110:113], v[178:181], v[154:157]
	ds_read_b128 v[158:161], v197 offset:0
	ds_read_b128 v[162:165], v197 offset:512
	ds_read_b128 v[166:169], v197 offset:1024
	ds_read_b128 v[170:173], v197 offset:1536
	s_waitcnt lgkmcnt(6)
	ds_read_b128 v[178:181], v194 offset:15376
	v_mfma_f32_16x16x32_f16 v[142:145], v[114:117], v[182:185], v[142:145]
	v_mfma_f32_16x16x32_f16 v[146:149], v[118:121], v[182:185], v[146:149]
	v_mfma_f32_16x16x32_f16 v[150:153], v[122:125], v[182:185], v[150:153]
	v_mfma_f32_16x16x32_f16 v[154:157], v[126:129], v[182:185], v[154:157]
	s_waitcnt lgkmcnt(6)
	ds_read_b128 v[182:185], v194 offset:15392
	s_waitcnt lgkmcnt(5)
	v_mfma_f32_16x16x32_f16 v[158:161], v[2:5], v[174:177], v[158:161]
	s_waitcnt lgkmcnt(4)
	v_mfma_f32_16x16x32_f16 v[162:165], v[6:9], v[174:177], v[162:165]
	s_waitcnt lgkmcnt(3)
	v_mfma_f32_16x16x32_f16 v[166:169], v[10:13], v[174:177], v[166:169]
	s_waitcnt lgkmcnt(2)
	v_mfma_f32_16x16x32_f16 v[170:173], v[14:17], v[174:177], v[170:173]
	s_waitcnt lgkmcnt(1)
	ds_read_b128 v[174:177], v194 offset:15408
	v_mfma_f32_16x16x32_f16 v[158:161], v[18:21], v[178:181], v[158:161]
	v_exp_f32_e32 v142, v142
	v_exp_f32_e32 v143, v143
	v_exp_f32_e32 v144, v144
	v_exp_f32_e32 v145, v145
	v_exp_f32_e32 v146, v146
	v_exp_f32_e32 v147, v147
	v_exp_f32_e32 v148, v148
	v_exp_f32_e32 v149, v149
	v_exp_f32_e32 v150, v150
	v_exp_f32_e32 v151, v151
	v_exp_f32_e32 v152, v152
	v_exp_f32_e32 v153, v153
	v_exp_f32_e32 v154, v154
	v_exp_f32_e32 v155, v155
	v_exp_f32_e32 v156, v156
	v_exp_f32_e32 v157, v157
	v_add_f32_e32 v150, 1.0, v150
	v_add_f32_e32 v151, 1.0, v151
	v_add_f32_e32 v152, 1.0, v152
	v_mfma_f32_16x16x32_f16 v[162:165], v[22:25], v[178:181], v[162:165]
	v_add_f32_e32 v153, 1.0, v153
	v_add_f32_e32 v146, 1.0, v146
	v_add_f32_e32 v147, 1.0, v147
	v_add_f32_e32 v148, 1.0, v148
	v_add_f32_e32 v149, 1.0, v149
	v_fma_f32 v142, v142, v150, v150
	v_fma_f32 v143, v143, v151, v151
	v_fma_f32 v144, v144, v152, v152
	v_fma_f32 v145, v145, v153, v153
	v_rcp_f32_e32 v146, v146
	v_rcp_f32_e32 v147, v147
	v_rcp_f32_e32 v148, v148
	v_rcp_f32_e32 v149, v149
	v_fma_f32 v150, v150, v204, s16
	v_fma_f32 v151, v151, v204, s16
	v_fma_f32 v152, v152, v204, s16
	v_fma_f32 v153, v153, v204, s16
	v_rcp_f32_e32 v142, v142
	v_rcp_f32_e32 v143, v143
	v_rcp_f32_e32 v144, v144
	v_mfma_f32_16x16x32_f16 v[166:169], v[26:29], v[178:181], v[166:169]
	v_rcp_f32_e32 v145, v145
	v_mul_f32_e32 v138, v138, v146
	v_mul_f32_e32 v139, v139, v147
	v_mul_f32_e32 v140, v140, v148
	v_mul_f32_e32 v141, v141, v149
	v_fma_f32 v138, v150, v142, v138
	v_fma_f32 v139, v151, v143, v139
	v_fma_f32 v140, v152, v144, v140
	v_fma_f32 v141, v153, v145, v141
	v_exp_f32_e32 v146, v138
	v_exp_f32_e32 v147, v139
	v_exp_f32_e32 v148, v140
	v_exp_f32_e32 v149, v141
	v_add_f32_e32 v142, 1.0, v146
	v_add_f32_e32 v143, 1.0, v147
	v_add_f32_e32 v144, 1.0, v148
	v_add_f32_e32 v145, 1.0, v149
	v_add_f32_e32 v150, -1.0, v146
	v_add_f32_e32 v151, -1.0, v147
	v_add_f32_e32 v152, -1.0, v148
	v_mfma_f32_16x16x32_f16 v[170:173], v[30:33], v[178:181], v[170:173]
	v_add_f32_e32 v153, -1.0, v149
	v_fma_f32 v154, v154, v142, v142
	v_fma_f32 v155, v155, v143, v143
	v_fma_f32 v156, v156, v144, v144
	v_fma_f32 v157, v157, v145, v145
	v_rcp_f32_e32 v154, v154
	v_rcp_f32_e32 v155, v155
	v_rcp_f32_e32 v156, v156
	v_rcp_f32_e32 v157, v157
	v_mul_f32_e32 v154, v150, v154
	v_mul_f32_e32 v155, v151, v155
	v_mul_f32_e32 v156, v152, v156
	v_mul_f32_e32 v157, v153, v157
	v_cvt_pk_f16_f32 v154, v154, v155
	v_cvt_pk_f16_f32 v155, v156, v157
	ds_write_b64 v196, v[154:155] offset:17920
	ds_read_b128 v[142:145], v197 offset:0
	ds_read_b128 v[146:149], v197 offset:512
	ds_read_b128 v[150:153], v197 offset:1024
	ds_read_b128 v[154:157], v197 offset:1536
	s_waitcnt lgkmcnt(0)
	s_barrier
	ds_read_b128 v[178:181], v195 offset:15360
	v_mfma_f32_16x16x32_f16 v[158:161], v[34:37], v[182:185], v[158:161]
	v_mfma_f32_16x16x32_f16 v[162:165], v[38:41], v[182:185], v[162:165]
	v_mfma_f32_16x16x32_f16 v[166:169], v[42:45], v[182:185], v[166:169]
	v_mfma_f32_16x16x32_f16 v[170:173], v[46:49], v[182:185], v[170:173]
	ds_read_b128 v[182:185], v195 offset:15376
	v_mfma_f32_16x16x32_f16 v[158:161], v[50:53], v[174:177], v[158:161]
	v_mfma_f32_16x16x32_f16 v[162:165], v[54:57], v[174:177], v[162:165]
	v_mfma_f32_16x16x32_f16 v[166:169], v[58:61], v[174:177], v[166:169]
	v_mfma_f32_16x16x32_f16 v[170:173], v[62:65], v[174:177], v[170:173]
	s_cmp_ge_u32 s24, 4
	s_cbranch_scc1 .Lskipx84
	s_cmp_eq_u32 s17, 14
	s_cbranch_scc1 .Lskipx84
	global_load_dwordx4 v[186:189], v198, s[12:13]
.Lskipx84:
	s_waitcnt lgkmcnt(1)
	ds_read_b128 v[174:177], v195 offset:15392
	v_mfma_f32_16x16x32_f16 v[158:161], v[66:69], v[178:181], v[158:161]
	v_mfma_f32_16x16x32_f16 v[162:165], v[70:73], v[178:181], v[162:165]
	v_mfma_f32_16x16x32_f16 v[166:169], v[74:77], v[178:181], v[166:169]
	v_mfma_f32_16x16x32_f16 v[170:173], v[78:81], v[178:181], v[170:173]
	global_load_dwordx4 v[190:193], v199, s[8:9]
	s_waitcnt lgkmcnt(1)
	ds_read_b128 v[178:181], v195 offset:15408
	v_mfma_f32_16x16x32_f16 v[158:161], v[82:85], v[182:185], v[158:161]
	v_mfma_f32_16x16x32_f16 v[162:165], v[86:89], v[182:185], v[162:165]
	v_mfma_f32_16x16x32_f16 v[166:169], v[90:93], v[182:185], v[166:169]
	v_mfma_f32_16x16x32_f16 v[170:173], v[94:97], v[182:185], v[170:173]
	s_add_u32 s12, s12, 0x271000
	s_waitcnt lgkmcnt(1)
	ds_read_b128 v[182:185], v194 offset:16640
	v_mfma_f32_16x16x32_f16 v[158:161], v[98:101], v[174:177], v[158:161]
	v_mfma_f32_16x16x32_f16 v[162:165], v[102:105], v[174:177], v[162:165]
	v_mfma_f32_16x16x32_f16 v[166:169], v[106:109], v[174:177], v[166:169]
	v_mfma_f32_16x16x32_f16 v[170:173], v[110:113], v[174:177], v[170:173]
	s_addc_u32 s13, s13, 0
	s_waitcnt lgkmcnt(1)
	ds_read_b128 v[174:177], v194 offset:16656
	v_mfma_f32_16x16x32_f16 v[158:161], v[114:117], v[178:181], v[158:161]
	v_mfma_f32_16x16x32_f16 v[162:165], v[118:121], v[178:181], v[162:165]
	s_add_u32 s8, s8, 0x271000
	v_mfma_f32_16x16x32_f16 v[166:169], v[122:125], v[178:181], v[166:169]
	v_mfma_f32_16x16x32_f16 v[170:173], v[126:129], v[178:181], v[170:173]
	s_addc_u32 s9, s9, 0
	s_waitcnt lgkmcnt(1)
	ds_read_b128 v[178:181], v195 offset:16640
	v_mfma_f32_16x16x32_f16 v[142:145], v[2:5], v[182:185], v[142:145]
	v_mfma_f32_16x16x32_f16 v[146:149], v[6:9], v[182:185], v[146:149]
	v_mfma_f32_16x16x32_f16 v[150:153], v[10:13], v[182:185], v[150:153]
	v_mfma_f32_16x16x32_f16 v[154:157], v[14:17], v[182:185], v[154:157]
	s_waitcnt lgkmcnt(1)
	ds_read_b128 v[182:185], v195 offset:16656
	v_mfma_f32_16x16x32_f16 v[142:145], v[18:21], v[174:177], v[142:145]
	v_mfma_f32_16x16x32_f16 v[146:149], v[22:25], v[174:177], v[146:149]
	v_mfma_f32_16x16x32_f16 v[150:153], v[26:29], v[174:177], v[150:153]
	v_mfma_f32_16x16x32_f16 v[154:157], v[30:33], v[174:177], v[154:157]
	s_waitcnt lgkmcnt(1)
	ds_read_b128 v[174:177], v194 offset:16672
	v_mfma_f32_16x16x32_f16 v[142:145], v[66:69], v[178:181], v[142:145]
	v_exp_f32_e32 v158, v158
	v_exp_f32_e32 v159, v159
	v_exp_f32_e32 v160, v160
	v_mfma_f32_16x16x32_f16 v[146:149], v[70:73], v[178:181], v[146:149]
	v_exp_f32_e32 v161, v161
	v_exp_f32_e32 v162, v162
	v_exp_f32_e32 v163, v163
	v_exp_f32_e32 v164, v164
	v_mfma_f32_16x16x32_f16 v[150:153], v[74:77], v[178:181], v[150:153]
	v_exp_f32_e32 v165, v165
	v_exp_f32_e32 v166, v166
	v_exp_f32_e32 v167, v167
	v_exp_f32_e32 v168, v168
	v_mfma_f32_16x16x32_f16 v[154:157], v[78:81], v[178:181], v[154:157]
	v_exp_f32_e32 v169, v169
	v_exp_f32_e32 v170, v170
	v_exp_f32_e32 v171, v171
	v_exp_f32_e32 v172, v172
	s_waitcnt lgkmcnt(1)
	ds_read_b128 v[178:181], v194 offset:16688
	v_mfma_f32_16x16x32_f16 v[142:145], v[82:85], v[182:185], v[142:145]
	v_exp_f32_e32 v173, v173
	v_add_f32_e32 v166, 1.0, v166
	v_add_f32_e32 v167, 1.0, v167
	v_add_f32_e32 v168, 1.0, v168
	v_mfma_f32_16x16x32_f16 v[146:149], v[86:89], v[182:185], v[146:149]
	v_add_f32_e32 v169, 1.0, v169
	v_add_f32_e32 v162, 1.0, v162
	v_add_f32_e32 v163, 1.0, v163
	v_add_f32_e32 v164, 1.0, v164
	v_mfma_f32_16x16x32_f16 v[150:153], v[90:93], v[182:185], v[150:153]
	v_add_f32_e32 v165, 1.0, v165
	v_fma_f32 v158, v158, v166, v166
	v_fma_f32 v159, v159, v167, v167
	v_fma_f32 v160, v160, v168, v168
	v_mfma_f32_16x16x32_f16 v[154:157], v[94:97], v[182:185], v[154:157]
	v_fma_f32 v161, v161, v169, v169
	v_rcp_f32_e32 v162, v162
	v_rcp_f32_e32 v163, v163
	v_rcp_f32_e32 v164, v164
	s_waitcnt lgkmcnt(1)
	ds_read_b128 v[182:185], v195 offset:16672
	v_mfma_f32_16x16x32_f16 v[142:145], v[34:37], v[174:177], v[142:145]
	v_rcp_f32_e32 v165, v165
	v_fma_f32 v166, v166, v204, s16
	v_fma_f32 v167, v167, v204, s16
	v_fma_f32 v168, v168, v204, s16
	v_mfma_f32_16x16x32_f16 v[146:149], v[38:41], v[174:177], v[146:149]
	v_fma_f32 v169, v169, v204, s16
	v_rcp_f32_e32 v158, v158
	v_rcp_f32_e32 v159, v159
	v_rcp_f32_e32 v160, v160
	v_mfma_f32_16x16x32_f16 v[150:153], v[42:45], v[174:177], v[150:153]
	v_rcp_f32_e32 v161, v161
	v_mul_f32_e32 v130, v130, v162
	v_mul_f32_e32 v131, v131, v163
	v_mul_f32_e32 v132, v132, v164
	v_mfma_f32_16x16x32_f16 v[154:157], v[46:49], v[174:177], v[154:157]
	v_mul_f32_e32 v133, v133, v165
	v_fma_f32 v130, v166, v158, v130
	v_fma_f32 v131, v167, v159, v131
	v_fma_f32 v132, v168, v160, v132
	s_waitcnt lgkmcnt(1)
	ds_read_b128 v[174:177], v195 offset:16688
	v_mfma_f32_16x16x32_f16 v[142:145], v[50:53], v[178:181], v[142:145]
	s_waitcnt vmcnt(0)
	s_cmp_ge_u32 s24, 4
	s_cbranch_scc1 .Lskips85
	ds_write_b128 v201, v[186:189] offset:15360
.Lskips85:
	ds_write_b128 v201, v[190:193] offset:1280
	v_fma_f32 v133, v169, v161, v133
	v_exp_f32_e32 v162, v130
	v_exp_f32_e32 v163, v131
	v_mfma_f32_16x16x32_f16 v[146:149], v[54:57], v[178:181], v[146:149]
	v_exp_f32_e32 v164, v132
	v_exp_f32_e32 v165, v133
	v_add_f32_e32 v158, 1.0, v162
	v_add_f32_e32 v159, 1.0, v163
	v_mfma_f32_16x16x32_f16 v[150:153], v[58:61], v[178:181], v[150:153]
	v_add_f32_e32 v160, 1.0, v164
	v_add_f32_e32 v161, 1.0, v165
	v_add_f32_e32 v166, -1.0, v162
	v_add_f32_e32 v167, -1.0, v163
	v_mfma_f32_16x16x32_f16 v[154:157], v[62:65], v[178:181], v[154:157]
	v_add_f32_e32 v168, -1.0, v164
	v_add_f32_e32 v169, -1.0, v165
	v_fma_f32 v170, v170, v158, v158
	v_fma_f32 v171, v171, v159, v159
	v_fma_f32 v172, v172, v160, v160
	s_waitcnt lgkmcnt(3)
	ds_read_b128 v[178:181], v194 offset:17920
	v_mfma_f32_16x16x32_f16 v[142:145], v[98:101], v[182:185], v[142:145]
	v_fma_f32 v173, v173, v161, v161
	v_rcp_f32_e32 v170, v170
	v_rcp_f32_e32 v171, v171
	v_rcp_f32_e32 v172, v172
	v_mfma_f32_16x16x32_f16 v[146:149], v[102:105], v[182:185], v[146:149]
	v_rcp_f32_e32 v173, v173
	v_mul_f32_e32 v170, v166, v170
	v_mul_f32_e32 v171, v167, v171
	v_mul_f32_e32 v172, v168, v172
	v_mfma_f32_16x16x32_f16 v[150:153], v[106:109], v[182:185], v[150:153]
	v_mul_f32_e32 v173, v169, v173
	v_cvt_pk_f16_f32 v170, v170, v171
	v_cvt_pk_f16_f32 v171, v172, v173
	ds_write_b64 v196, v[170:171] offset:0
	v_mfma_f32_16x16x32_f16 v[154:157], v[110:113], v[182:185], v[154:157]
	ds_read_b128 v[158:161], v197 offset:0
	ds_read_b128 v[162:165], v197 offset:512
	ds_read_b128 v[166:169], v197 offset:1024
	ds_read_b128 v[170:173], v197 offset:1536
	s_waitcnt lgkmcnt(8)
	ds_read_b128 v[182:185], v194 offset:17936
	v_mfma_f32_16x16x32_f16 v[142:145], v[114:117], v[174:177], v[142:145]
	v_mfma_f32_16x16x32_f16 v[146:149], v[118:121], v[174:177], v[146:149]
	v_mfma_f32_16x16x32_f16 v[150:153], v[122:125], v[174:177], v[150:153]
	v_mfma_f32_16x16x32_f16 v[154:157], v[126:129], v[174:177], v[154:157]
	s_waitcnt lgkmcnt(6)
	ds_read_b128 v[174:177], v195 offset:17920
	s_waitcnt lgkmcnt(5)
	v_mfma_f32_16x16x32_f16 v[158:161], v[2:5], v[178:181], v[158:161]
	s_waitcnt lgkmcnt(4)
	v_mfma_f32_16x16x32_f16 v[162:165], v[6:9], v[178:181], v[162:165]
	s_waitcnt lgkmcnt(3)
	v_mfma_f32_16x16x32_f16 v[166:169], v[10:13], v[178:181], v[166:169]
	s_waitcnt lgkmcnt(2)
	v_mfma_f32_16x16x32_f16 v[170:173], v[14:17], v[178:181], v[170:173]
	s_waitcnt lgkmcnt(1)
	ds_read_b128 v[178:181], v195 offset:17936
	v_mfma_f32_16x16x32_f16 v[158:161], v[18:21], v[182:185], v[158:161]
	v_mfma_f32_16x16x32_f16 v[162:165], v[22:25], v[182:185], v[162:165]
	v_mfma_f32_16x16x32_f16 v[166:169], v[26:29], v[182:185], v[166:169]
	v_mfma_f32_16x16x32_f16 v[170:173], v[30:33], v[182:185], v[170:173]
	s_waitcnt lgkmcnt(1)
	ds_read_b128 v[182:185], v194 offset:17952
	v_mfma_f32_16x16x32_f16 v[158:161], v[66:69], v[174:177], v[158:161]
	v_exp_f32_e32 v142, v142
	v_exp_f32_e32 v143, v143
	v_exp_f32_e32 v144, v144
	v_mfma_f32_16x16x32_f16 v[162:165], v[70:73], v[174:177], v[162:165]
	v_exp_f32_e32 v145, v145
	v_exp_f32_e32 v146, v146
	v_exp_f32_e32 v147, v147
	v_exp_f32_e32 v148, v148
	v_mfma_f32_16x16x32_f16 v[166:169], v[74:77], v[174:177], v[166:169]
	v_exp_f32_e32 v149, v149
	v_exp_f32_e32 v150, v150
	v_exp_f32_e32 v151, v151
	v_exp_f32_e32 v152, v152
	v_mfma_f32_16x16x32_f16 v[170:173], v[78:81], v[174:177], v[170:173]
	v_exp_f32_e32 v153, v153
	v_exp_f32_e32 v154, v154
	v_exp_f32_e32 v155, v155
	v_exp_f32_e32 v156, v156
	s_waitcnt lgkmcnt(1)
	ds_read_b128 v[174:177], v194 offset:17968
	v_mfma_f32_16x16x32_f16 v[158:161], v[82:85], v[178:181], v[158:161]
	v_exp_f32_e32 v157, v157
	v_add_f32_e32 v150, 1.0, v150
	v_add_f32_e32 v151, 1.0, v151
	v_add_f32_e32 v152, 1.0, v152
	v_mfma_f32_16x16x32_f16 v[162:165], v[86:89], v[178:181], v[162:165]
	v_add_f32_e32 v153, 1.0, v153
	v_add_f32_e32 v146, 1.0, v146
	v_add_f32_e32 v147, 1.0, v147
	v_add_f32_e32 v148, 1.0, v148
	v_mfma_f32_16x16x32_f16 v[166:169], v[90:93], v[178:181], v[166:169]
	v_add_f32_e32 v149, 1.0, v149
	v_fma_f32 v142, v142, v150, v150
	v_fma_f32 v143, v143, v151, v151
	v_fma_f32 v144, v144, v152, v152
	v_mfma_f32_16x16x32_f16 v[170:173], v[94:97], v[178:181], v[170:173]
	v_fma_f32 v145, v145, v153, v153
	v_rcp_f32_e32 v146, v146
	v_rcp_f32_e32 v147, v147
	v_rcp_f32_e32 v148, v148
	s_waitcnt lgkmcnt(1)
	ds_read_b128 v[178:181], v195 offset:17952
	v_mfma_f32_16x16x32_f16 v[158:161], v[34:37], v[182:185], v[158:161]
	v_rcp_f32_e32 v149, v149
	v_fma_f32 v150, v150, v204, s16
	v_fma_f32 v151, v151, v204, s16
	v_fma_f32 v152, v152, v204, s16
	v_mfma_f32_16x16x32_f16 v[162:165], v[38:41], v[182:185], v[162:165]
	v_fma_f32 v153, v153, v204, s16
	v_rcp_f32_e32 v142, v142
	v_rcp_f32_e32 v143, v143
	v_rcp_f32_e32 v144, v144
	v_mfma_f32_16x16x32_f16 v[166:169], v[42:45], v[182:185], v[166:169]
	v_rcp_f32_e32 v145, v145
	v_mul_f32_e32 v134, v134, v146
	v_mul_f32_e32 v135, v135, v147
	v_mul_f32_e32 v136, v136, v148
	v_mfma_f32_16x16x32_f16 v[170:173], v[46:49], v[182:185], v[170:173]
	v_mul_f32_e32 v137, v137, v149
	v_fma_f32 v134, v150, v142, v134
	v_fma_f32 v135, v151, v143, v135
	v_fma_f32 v136, v152, v144, v136
	s_waitcnt lgkmcnt(1)
	ds_read_b128 v[182:185], v195 offset:17968
	v_mfma_f32_16x16x32_f16 v[158:161], v[50:53], v[174:177], v[158:161]
	v_fma_f32 v137, v153, v145, v137
	v_exp_f32_e32 v146, v134
	v_exp_f32_e32 v147, v135
	v_exp_f32_e32 v148, v136
	v_mfma_f32_16x16x32_f16 v[162:165], v[54:57], v[174:177], v[162:165]
	v_exp_f32_e32 v149, v137
	v_add_f32_e32 v142, 1.0, v146
	v_add_f32_e32 v143, 1.0, v147
	v_add_f32_e32 v144, 1.0, v148
	v_mfma_f32_16x16x32_f16 v[166:169], v[58:61], v[174:177], v[166:169]
	v_add_f32_e32 v145, 1.0, v149
	v_add_f32_e32 v150, -1.0, v146
	v_add_f32_e32 v151, -1.0, v147
	v_add_f32_e32 v152, -1.0, v148
	v_mfma_f32_16x16x32_f16 v[170:173], v[62:65], v[174:177], v[170:173]
	v_add_f32_e32 v153, -1.0, v149
	v_fma_f32 v154, v154, v142, v142
	v_fma_f32 v155, v155, v143, v143
	v_fma_f32 v156, v156, v144, v144
	s_waitcnt lgkmcnt(1)
	ds_read_b128 v[174:177], v194 offset:0
	v_mfma_f32_16x16x32_f16 v[158:161], v[98:101], v[178:181], v[158:161]
	v_fma_f32 v157, v157, v145, v145
	v_rcp_f32_e32 v154, v154
	v_rcp_f32_e32 v155, v155
	v_rcp_f32_e32 v156, v156
	v_mfma_f32_16x16x32_f16 v[162:165], v[102:105], v[178:181], v[162:165]
	v_rcp_f32_e32 v157, v157
	v_mul_f32_e32 v154, v150, v154
	v_mul_f32_e32 v155, v151, v155
	v_mul_f32_e32 v156, v152, v156
	v_mfma_f32_16x16x32_f16 v[166:169], v[106:109], v[178:181], v[166:169]
	v_mul_f32_e32 v157, v153, v157
	v_cvt_pk_f16_f32 v154, v154, v155
	v_cvt_pk_f16_f32 v155, v156, v157
	ds_write_b64 v196, v[154:155] offset:1280
	v_mfma_f32_16x16x32_f16 v[170:173], v[110:113], v[178:181], v[170:173]
	ds_read_b128 v[142:145], v197 offset:0
	ds_read_b128 v[146:149], v197 offset:512
	ds_read_b128 v[150:153], v197 offset:1024
	ds_read_b128 v[154:157], v197 offset:1536
	s_waitcnt lgkmcnt(6)
	ds_read_b128 v[178:181], v194 offset:16
	v_mfma_f32_16x16x32_f16 v[158:161], v[114:117], v[182:185], v[158:161]
	v_mfma_f32_16x16x32_f16 v[162:165], v[118:121], v[182:185], v[162:165]
	v_mfma_f32_16x16x32_f16 v[166:169], v[122:125], v[182:185], v[166:169]
	v_mfma_f32_16x16x32_f16 v[170:173], v[126:129], v[182:185], v[170:173]
	s_waitcnt lgkmcnt(6)
	ds_read_b128 v[182:185], v194 offset:32
	s_waitcnt lgkmcnt(5)
	v_mfma_f32_16x16x32_f16 v[142:145], v[2:5], v[174:177], v[142:145]
	s_waitcnt lgkmcnt(4)
	v_mfma_f32_16x16x32_f16 v[146:149], v[6:9], v[174:177], v[146:149]
	s_waitcnt lgkmcnt(3)
	v_mfma_f32_16x16x32_f16 v[150:153], v[10:13], v[174:177], v[150:153]
	s_waitcnt lgkmcnt(2)
	v_mfma_f32_16x16x32_f16 v[154:157], v[14:17], v[174:177], v[154:157]
	s_waitcnt lgkmcnt(1)
	ds_read_b128 v[174:177], v194 offset:48
	v_mfma_f32_16x16x32_f16 v[142:145], v[18:21], v[178:181], v[142:145]
	v_exp_f32_e32 v158, v158
	v_exp_f32_e32 v159, v159
	v_exp_f32_e32 v160, v160
	v_exp_f32_e32 v161, v161
	v_exp_f32_e32 v162, v162
	v_exp_f32_e32 v163, v163
	v_exp_f32_e32 v164, v164
	v_exp_f32_e32 v165, v165
	v_exp_f32_e32 v166, v166
	v_exp_f32_e32 v167, v167
	v_exp_f32_e32 v168, v168
	v_exp_f32_e32 v169, v169
	v_exp_f32_e32 v170, v170
	v_exp_f32_e32 v171, v171
	v_exp_f32_e32 v172, v172
	v_exp_f32_e32 v173, v173
	v_add_f32_e32 v166, 1.0, v166
	v_add_f32_e32 v167, 1.0, v167
	v_add_f32_e32 v168, 1.0, v168
	v_mfma_f32_16x16x32_f16 v[146:149], v[22:25], v[178:181], v[146:149]
	v_add_f32_e32 v169, 1.0, v169
	v_add_f32_e32 v162, 1.0, v162
	v_add_f32_e32 v163, 1.0, v163
	v_add_f32_e32 v164, 1.0, v164
	v_add_f32_e32 v165, 1.0, v165
	v_fma_f32 v158, v158, v166, v166
	v_fma_f32 v159, v159, v167, v167
	v_fma_f32 v160, v160, v168, v168
	v_fma_f32 v161, v161, v169, v169
	v_rcp_f32_e32 v162, v162
	v_rcp_f32_e32 v163, v163
	v_rcp_f32_e32 v164, v164
	v_rcp_f32_e32 v165, v165
	v_fma_f32 v166, v166, v204, s16
	v_fma_f32 v167, v167, v204, s16
	v_fma_f32 v168, v168, v204, s16
	v_fma_f32 v169, v169, v204, s16
	v_rcp_f32_e32 v158, v158
	v_rcp_f32_e32 v159, v159
	v_rcp_f32_e32 v160, v160
	v_mfma_f32_16x16x32_f16 v[150:153], v[26:29], v[178:181], v[150:153]
	v_rcp_f32_e32 v161, v161
	v_mul_f32_e32 v138, v138, v162
	v_mul_f32_e32 v139, v139, v163
	v_mul_f32_e32 v140, v140, v164
	v_mul_f32_e32 v141, v141, v165
	v_fma_f32 v138, v166, v158, v138
	v_fma_f32 v139, v167, v159, v139
	v_fma_f32 v140, v168, v160, v140
	v_fma_f32 v141, v169, v161, v141
	v_exp_f32_e32 v162, v138
	v_exp_f32_e32 v163, v139
	v_exp_f32_e32 v164, v140
	v_exp_f32_e32 v165, v141
	v_add_f32_e32 v158, 1.0, v162
	v_add_f32_e32 v159, 1.0, v163
	v_add_f32_e32 v160, 1.0, v164
	v_add_f32_e32 v161, 1.0, v165
	v_add_f32_e32 v166, -1.0, v162
	v_add_f32_e32 v167, -1.0, v163
	v_add_f32_e32 v168, -1.0, v164
	v_mfma_f32_16x16x32_f16 v[154:157], v[30:33], v[178:181], v[154:157]
	v_add_f32_e32 v169, -1.0, v165
	v_fma_f32 v170, v170, v158, v158
	v_fma_f32 v171, v171, v159, v159
	v_fma_f32 v172, v172, v160, v160
	v_fma_f32 v173, v173, v161, v161
	v_rcp_f32_e32 v170, v170
	v_rcp_f32_e32 v171, v171
	v_rcp_f32_e32 v172, v172
	v_rcp_f32_e32 v173, v173
	v_mul_f32_e32 v170, v166, v170
	v_mul_f32_e32 v171, v167, v171
	v_mul_f32_e32 v172, v168, v172
	v_mul_f32_e32 v173, v169, v173
	v_cvt_pk_f16_f32 v170, v170, v171
	v_cvt_pk_f16_f32 v171, v172, v173
	ds_write_b64 v196, v[170:171] offset:2560
	ds_read_b128 v[158:161], v197 offset:0
	ds_read_b128 v[162:165], v197 offset:512
	ds_read_b128 v[166:169], v197 offset:1024
	ds_read_b128 v[170:173], v197 offset:1536
	s_waitcnt lgkmcnt(0)
	s_barrier
	s_add_u32 s17, s17, 2
	s_cmp_lt_u32 s17, 16
	s_cbranch_scc1 .Llstm2_loop
	s_waitcnt lgkmcnt(0)
	s_load_dwordx2 s[4:5], s[0:1], 0x38
	s_load_dwordx2 s[6:7], s[0:1], 0x40
	s_load_dwordx2 s[8:9], s[0:1], 0x48
	s_load_dwordx2 s[10:11], s[0:1], 0x50
	s_load_dwordx2 s[12:13], s[0:1], 0x58
	s_load_dwordx2 s[14:15], s[0:1], 0x60
	v_and_b32_e32 v1, 15, v0
	v_bfe_u32 v205, v0, 4, 2
	v_lshrrev_b32_e32 v206, 6, v0
	s_mul_i32 s22, s2, 48
	v_lshl_add_u32 v200, v206, 2, v205
	v_lshlrev_b32_e32 v200, 4, v200
	v_add_u32_e32 v198, s22, v1
	s_waitcnt lgkmcnt(0)
	v_min_u32_e32 v199, 0x270f, v198
	v_lshl_add_u32 v199, v199, 9, v200
	global_load_dwordx4 v[142:145], v199, s[14:15]
	v_add_u32_e32 v198, 16, v198
	v_min_u32_e32 v199, 0x270f, v198
	v_lshl_add_u32 v199, v199, 9, v200
	global_load_dwordx4 v[146:149], v199, s[14:15]
	v_add_u32_e32 v198, 16, v198
	v_min_u32_e32 v199, 0x270f, v198
	v_lshl_add_u32 v199, v199, 9, v200
	global_load_dwordx4 v[150:153], v199, s[14:15]
	global_load_dwordx4 v[158:161], v200, s[6:7]
	global_load_dwordx4 v[162:165], v200, s[8:9]
	v_and_b32_e32 v1, 63, v0
	v_lshlrev_b32_e32 v1, 4, v1
	v_lshl_add_u32 v1, v206, 10, v1
	global_load_dwordx4 v[2:5], v1, s[4:5]
	v_add_u32_e32 v1, 0x2000, v1
	global_load_dwordx4 v[6:9], v1, s[4:5]
	v_add_u32_e32 v1, 0x2000, v1
	global_load_dwordx4 v[10:13], v1, s[4:5]
	v_add_u32_e32 v1, 0x2000, v1
	global_load_dwordx4 v[14:17], v1, s[4:5]
	v_add_u32_e32 v1, 0x2000, v1
	global_load_dwordx4 v[18:21], v1, s[4:5]
	v_add_u32_e32 v1, 0x2000, v1
	global_load_dwordx4 v[22:25], v1, s[4:5]
	v_add_u32_e32 v1, 0x2000, v1
	global_load_dwordx4 v[26:29], v1, s[4:5]
	v_add_u32_e32 v1, 0x2000, v1
	global_load_dwordx4 v[30:33], v1, s[4:5]
	s_waitcnt vmcnt(0)
	ds_read_b128 v[174:177], v207 offset:0
	ds_read_b128 v[178:181], v207 offset:1280
	ds_read_b128 v[182:185], v207 offset:2560
	s_waitcnt lgkmcnt(2)
	v_mfma_f32_16x16x32_f16 v[142:145], v[2:5], v[174:177], v[142:145]
	ds_read_b128 v[174:177], v207 offset:16
	s_waitcnt lgkmcnt(2)
	v_mfma_f32_16x16x32_f16 v[146:149], v[2:5], v[178:181], v[146:149]
	ds_read_b128 v[178:181], v207 offset:1296
	s_waitcnt lgkmcnt(2)
	v_mfma_f32_16x16x32_f16 v[150:153], v[2:5], v[182:185], v[150:153]
	ds_read_b128 v[182:185], v207 offset:2576
	s_waitcnt lgkmcnt(2)
	v_mfma_f32_16x16x32_f16 v[142:145], v[6:9], v[174:177], v[142:145]
	ds_read_b128 v[174:177], v207 offset:32
	s_waitcnt lgkmcnt(2)
	v_mfma_f32_16x16x32_f16 v[146:149], v[6:9], v[178:181], v[146:149]
	ds_read_b128 v[178:181], v207 offset:1312
	s_waitcnt lgkmcnt(2)
	v_mfma_f32_16x16x32_f16 v[150:153], v[6:9], v[182:185], v[150:153]
	ds_read_b128 v[182:185], v207 offset:2592
	s_waitcnt lgkmcnt(2)
	v_mfma_f32_16x16x32_f16 v[142:145], v[10:13], v[174:177], v[142:145]
	ds_read_b128 v[174:177], v207 offset:48
	s_waitcnt lgkmcnt(2)
	v_mfma_f32_16x16x32_f16 v[146:149], v[10:13], v[178:181], v[146:149]
	ds_read_b128 v[178:181], v207 offset:1328
	s_waitcnt lgkmcnt(2)
	v_mfma_f32_16x16x32_f16 v[150:153], v[10:13], v[182:185], v[150:153]
	ds_read_b128 v[182:185], v207 offset:2608
	s_waitcnt lgkmcnt(2)
	v_mfma_f32_16x16x32_f16 v[142:145], v[14:17], v[174:177], v[142:145]
	ds_read_b128 v[174:177], v195 offset:0
	s_waitcnt lgkmcnt(2)
	v_mfma_f32_16x16x32_f16 v[146:149], v[14:17], v[178:181], v[146:149]
	ds_read_b128 v[178:181], v195 offset:1280
	s_waitcnt lgkmcnt(2)
	v_mfma_f32_16x16x32_f16 v[150:153], v[14:17], v[182:185], v[150:153]
	ds_read_b128 v[182:185], v195 offset:2560
	s_waitcnt lgkmcnt(2)
	v_mfma_f32_16x16x32_f16 v[142:145], v[18:21], v[174:177], v[142:145]
	ds_read_b128 v[174:177], v195 offset:16
	s_waitcnt lgkmcnt(2)
	v_mfma_f32_16x16x32_f16 v[146:149], v[18:21], v[178:181], v[146:149]
	ds_read_b128 v[178:181], v195 offset:1296
	s_waitcnt lgkmcnt(2)
	v_mfma_f32_16x16x32_f16 v[150:153], v[18:21], v[182:185], v[150:153]
	ds_read_b128 v[182:185], v195 offset:2576
	s_waitcnt lgkmcnt(2)
	v_mfma_f32_16x16x32_f16 v[142:145], v[22:25], v[174:177], v[142:145]
	ds_read_b128 v[174:177], v195 offset:32
	s_waitcnt lgkmcnt(2)
	v_mfma_f32_16x16x32_f16 v[146:149], v[22:25], v[178:181], v[146:149]
	ds_read_b128 v[178:181], v195 offset:1312
	s_waitcnt lgkmcnt(2)
	v_mfma_f32_16x16x32_f16 v[150:153], v[22:25], v[182:185], v[150:153]
	ds_read_b128 v[182:185], v195 offset:2592
	s_waitcnt lgkmcnt(2)
	v_mfma_f32_16x16x32_f16 v[142:145], v[26:29], v[174:177], v[142:145]
	ds_read_b128 v[174:177], v195 offset:48
	s_waitcnt lgkmcnt(2)
	v_mfma_f32_16x16x32_f16 v[146:149], v[26:29], v[178:181], v[146:149]
	ds_read_b128 v[178:181], v195 offset:1328
	s_waitcnt lgkmcnt(2)
	v_mfma_f32_16x16x32_f16 v[150:153], v[26:29], v[182:185], v[150:153]
	ds_read_b128 v[182:185], v195 offset:2608
	s_waitcnt lgkmcnt(2)
	v_mfma_f32_16x16x32_f16 v[142:145], v[30:33], v[174:177], v[142:145]
	s_waitcnt lgkmcnt(1)
	v_mfma_f32_16x16x32_f16 v[146:149], v[30:33], v[178:181], v[146:149]
	s_waitcnt lgkmcnt(0)
	v_mfma_f32_16x16x32_f16 v[150:153], v[30:33], v[182:185], v[150:153]
	s_nop 7
	s_nop 1
	v_add_f32_e32 v142, v142, v158
	v_add_f32_e32 v143, v143, v159
	v_add_f32_e32 v144, v144, v160
	v_add_f32_e32 v145, v145, v161
	v_max_f32_e32 v142, 0, v142
	v_max_f32_e32 v143, 0, v143
	v_max_f32_e32 v144, 0, v144
	v_max_f32_e32 v145, 0, v145
	v_mul_f32_e32 v166, v142, v162
	v_fma_f32 v166, v143, v163, v166
	v_fma_f32 v166, v144, v164, v166
	v_fma_f32 v166, v145, v165, v166
	ds_write_b32 v208, v166 offset:0
	v_add_f32_e32 v146, v146, v158
	v_add_f32_e32 v147, v147, v159
	v_add_f32_e32 v148, v148, v160
	v_add_f32_e32 v149, v149, v161
	v_max_f32_e32 v146, 0, v146
	v_max_f32_e32 v147, 0, v147
	v_max_f32_e32 v148, 0, v148
	v_max_f32_e32 v149, 0, v149
	v_mul_f32_e32 v167, v146, v162
	v_fma_f32 v167, v147, v163, v167
	v_fma_f32 v167, v148, v164, v167
	v_fma_f32 v167, v149, v165, v167
	ds_write_b32 v208, v167 offset:2048
	v_add_f32_e32 v150, v150, v158
	v_add_f32_e32 v151, v151, v159
	v_add_f32_e32 v152, v152, v160
	v_add_f32_e32 v153, v153, v161
	v_max_f32_e32 v150, 0, v150
	v_max_f32_e32 v151, 0, v151
	v_max_f32_e32 v152, 0, v152
	v_max_f32_e32 v153, 0, v153
	v_mul_f32_e32 v168, v150, v162
	v_fma_f32 v168, v151, v163, v168
	v_fma_f32 v168, v152, v164, v168
	v_fma_f32 v168, v153, v165, v168
	ds_write_b32 v208, v168 offset:4096
	s_waitcnt lgkmcnt(0)
	s_barrier
	v_add_u32_e32 v205, s22, v0
	s_movk_i32 s23, 0x2710
	v_cmp_gt_u32_e64 s[16:17], s23, v205
	v_cmp_gt_u32_e64 s[18:19], 48, v0
	s_nop 3
	s_and_b64 s[16:17], s[16:17], s[18:19]
	s_and_saveexec_b64 s[18:19], s[16:17]
	s_cbranch_execz .Ll2_end
	v_lshlrev_b32_e32 v1, 7, v0
	v_add_u32_e32 v1, 0x13400, v1
	ds_read_b128 v[2:5], v1 offset:0
	ds_read_b128 v[6:9], v1 offset:16
	ds_read_b128 v[10:13], v1 offset:32
	ds_read_b128 v[14:17], v1 offset:48
	ds_read_b128 v[18:21], v1 offset:64
	ds_read_b128 v[22:25], v1 offset:80
	ds_read_b128 v[26:29], v1 offset:96
	ds_read_b128 v[30:33], v1 offset:112
	s_load_dword s20, s[10:11], 0x0
	s_waitcnt lgkmcnt(0)
	v_mov_b32_e32 v206, s20
	v_add_f32_e32 v206, v206, v2
	v_add_f32_e32 v206, v206, v3
	v_add_f32_e32 v206, v206, v4
	v_add_f32_e32 v206, v206, v5
	v_add_f32_e32 v206, v206, v6
	v_add_f32_e32 v206, v206, v7
	v_add_f32_e32 v206, v206, v8
	v_add_f32_e32 v206, v206, v9
	v_add_f32_e32 v206, v206, v10
	v_add_f32_e32 v206, v206, v11
	v_add_f32_e32 v206, v206, v12
	v_add_f32_e32 v206, v206, v13
	v_add_f32_e32 v206, v206, v14
	v_add_f32_e32 v206, v206, v15
	v_add_f32_e32 v206, v206, v16
	v_add_f32_e32 v206, v206, v17
	v_add_f32_e32 v206, v206, v18
	v_add_f32_e32 v206, v206, v19
	v_add_f32_e32 v206, v206, v20
	v_add_f32_e32 v206, v206, v21
	v_add_f32_e32 v206, v206, v22
	v_add_f32_e32 v206, v206, v23
	v_add_f32_e32 v206, v206, v24
	v_add_f32_e32 v206, v206, v25
	v_add_f32_e32 v206, v206, v26
	v_add_f32_e32 v206, v206, v27
	v_add_f32_e32 v206, v206, v28
	v_add_f32_e32 v206, v206, v29
	v_add_f32_e32 v206, v206, v30
	v_add_f32_e32 v206, v206, v31
	v_add_f32_e32 v206, v206, v32
	v_add_f32_e32 v206, v206, v33
	v_max_f32_e32 v206, 0, v206
	v_lshlrev_b32_e32 v205, 2, v205
	global_store_dword v205, v206, s[12:13]
